# v21 + first-K-tile fragment reads issued at the unit top, in front of the next-unit decode (all five GEMM instances)
# speedup vs baseline: 1.0056x; 1.0013x over previous
.LBB0_306:
	v_add_u32_e32 v132, 0x10000, v136
	v_add_u32_e32 v138, 0x14000, v136
	ds_read_b128 v[140:143], v132
	ds_read_b128 v[144:147], v132 offset:1024
	ds_read_b128 v[148:151], v132 offset:2048
	ds_read_b128 v[152:155], v132 offset:3072
	ds_read_b128 v[156:159], v138
	ds_read_b128 v[160:163], v138 offset:1024
	ds_read_b128 v[164:167], v138 offset:2048
	ds_read_b128 v[168:171], v138 offset:3072
	ds_read_b128 v[172:175], v137
	ds_read_b128 v[176:179], v137 offset:1024
	ds_read_b128 v[180:183], v137 offset:2048
	ds_read_b128 v[184:187], v137 offset:3072
	ds_read_b128 v[188:191], v137 offset:4096
	ds_read_b128 v[194:197], v137 offset:5120
	ds_read_b128 v[202:205], v137 offset:6144
	ds_read_b128 v[206:209], v137 offset:7168
	s_add_i32 s58, s58, 1
	v_readlane_b32 s0, v254, 38
	s_mul_i32 s0, s58, s0
	s_mul_hi_u32 s1, s58, s70
	s_add_i32 s1, s1, s0
	s_mul_i32 s0, s58, s70
	v_readlane_b32 s2, v255, 0
	s_add_u32 s2, s0, s2
	s_addc_u32 s3, s1, s48
	v_mov_b64_e32 v[0:1], 0x6e8
	v_cmp_lt_i64_e64 s[0:1], s[2:3], v[0:1]
	v_mov_b64_e32 v[0:1], 0x6e7
	v_cmp_gt_i64_e32 vcc, s[2:3], v[0:1]
	s_nop 3
	s_cmp_lg_u64 s[0:1], 0
	s_cselect_b64 s[100:101], -1, 1
	s_cbranch_vccnz .LBB0_308
	s_ashr_i32 s3, s2, 31
	s_lshr_b32 s3, s3, 29
	s_add_i32 s3, s2, s3
	s_ashr_i32 s16, s3, 3
	s_and_b32 s3, s3, -8
	s_sub_i32 s2, s2, s3
	s_cmp_lt_i32 s2, 0
	s_movk_i32 s3, 0xde
	s_cselect_b32 s3, s3, 0xdd
	s_mul_i32 s2, s2, s3
	s_add_i32 s2, s2, s16
	s_mul_hi_i32 s3, s2, 0x4ec4ec4f
	s_lshr_b32 s16, s3, 31
	s_ashr_i32 s3, s3, 5
	s_add_i32 s3, s3, s16
	s_lshl_b32 s17, s3, 3
	s_sub_i32 s16, 0x88, s17
	s_min_i32 s18, s16, 8
	s_abs_i32 s16, s18
	v_cvt_f32_u32_e32 v0, s16
	s_sub_i32 s21, 0, s16
	s_mulk_i32 s3, 0x68
	s_sub_i32 s2, s2, s3
	v_rcp_iflag_f32_e32 v0, v0
	s_abs_i32 s3, s2
	s_xor_b32 s19, s2, s18
	s_ashr_i32 s19, s19, 31
	v_mul_f32_e32 v0, 0x4f7ffffe, v0
	v_cvt_u32_f32_e32 v0, v0
	s_nop 0
	v_readfirstlane_b32 s26, v0
	s_mul_i32 s21, s21, s26
	s_mul_hi_u32 s21, s26, s21
	s_add_i32 s26, s26, s21
	s_mul_hi_u32 s21, s3, s26
	s_mul_i32 s26, s21, s16
	s_sub_i32 s3, s3, s26
	s_add_i32 s27, s21, 1
	s_sub_i32 s26, s3, s16
	s_cmp_ge_u32 s3, s16
	s_cselect_b32 s21, s27, s21
	s_cselect_b32 s3, s26, s3
	s_add_i32 s26, s21, 1
	s_cmp_ge_u32 s3, s16
	s_cselect_b32 s3, s26, s21
	s_xor_b32 s3, s3, s19
	s_sub_i32 s16, s3, s19
	s_mul_i32 s3, s16, s18
	s_sub_i32 s2, s2, s3
	s_add_i32 s18, s17, s2
.LBB0_308:
	v_mov_b32_e32 v0, 0
	s_mov_b32 s17, -2
	s_mov_b64 s[2:3], 0
	v_mov_b32_e32 v1, v0
	s_waitcnt lgkmcnt(0)
	s_add_u32 s33, s22, s2
	s_addc_u32 s61, s23, s3
	s_add_u32 s34, s33, 0x100
	s_addc_u32 s35, s61, 0
	s_add_u32 s26, s33, 0x180
	s_addc_u32 s27, s61, 0
	s_add_u32 s19, s24, s2
	s_addc_u32 s21, s25, s3
	s_add_u32 s36, s19, 0x100
	s_addc_u32 s37, s21, 0
	s_add_u32 s62, s33, 0x40080
	s_addc_u32 s63, s61, 0
	s_mov_b32 m0, s57
	s_nop 0
	global_load_lds_dwordx4 v65, s[62:63]
	s_nop 0
	s_mov_b32 m0, s59
	s_nop 0
	global_load_lds_dwordx4 v134, s[62:63]
	s_waitcnt vmcnt(8)
	s_waitcnt lgkmcnt(0)
	s_barrier
	s_setprio 1
	s_waitcnt lgkmcnt(0)
	v_mfma_f32_16x16x32_bf16 v[128:131], v[140:143], v[172:175], 0
	v_mfma_f32_16x16x32_bf16 v[124:127], v[148:151], v[172:175], 0
	v_mfma_f32_16x16x32_bf16 v[120:123], v[140:143], v[180:183], 0
	v_mfma_f32_16x16x32_bf16 v[116:119], v[148:151], v[180:183], 0
	v_mfma_f32_16x16x32_bf16 v[110:113], v[140:143], v[188:191], 0
	v_mfma_f32_16x16x32_bf16 v[106:109], v[148:151], v[188:191], 0
	v_mfma_f32_16x16x32_bf16 v[102:105], v[140:143], v[202:205], 0
	v_mfma_f32_16x16x32_bf16 v[98:101], v[148:151], v[202:205], 0
	v_mfma_f32_16x16x32_bf16 v[128:131], v[144:147], v[176:179], v[128:131]
	v_mfma_f32_16x16x32_bf16 v[124:127], v[152:155], v[176:179], v[124:127]
	v_mfma_f32_16x16x32_bf16 v[120:123], v[144:147], v[184:187], v[120:123]
	v_mfma_f32_16x16x32_bf16 v[116:119], v[152:155], v[184:187], v[116:119]
	v_mfma_f32_16x16x32_bf16 v[110:113], v[144:147], v[194:197], v[110:113]
	v_mfma_f32_16x16x32_bf16 v[106:109], v[152:155], v[194:197], v[106:109]
	v_mfma_f32_16x16x32_bf16 v[102:105], v[144:147], v[206:209], v[102:105]
	v_mfma_f32_16x16x32_bf16 v[98:101], v[152:155], v[206:209], v[98:101]
	s_setprio 0
	s_setprio 1
	v_mfma_f32_16x16x32_bf16 v[94:97], v[156:159], v[172:175], 0
	v_mfma_f32_16x16x32_bf16 v[90:93], v[164:167], v[172:175], 0
	v_mfma_f32_16x16x32_bf16 v[86:89], v[156:159], v[180:183], 0
	v_mfma_f32_16x16x32_bf16 v[82:85], v[164:167], v[180:183], 0
	v_mfma_f32_16x16x32_bf16 v[78:81], v[156:159], v[188:191], 0
	v_mfma_f32_16x16x32_bf16 v[74:77], v[164:167], v[188:191], 0
	v_mfma_f32_16x16x32_bf16 v[70:73], v[156:159], v[202:205], 0
	v_mfma_f32_16x16x32_bf16 v[66:69], v[164:167], v[202:205], 0
	v_mfma_f32_16x16x32_bf16 v[94:97], v[160:163], v[176:179], v[94:97]
	v_mfma_f32_16x16x32_bf16 v[90:93], v[168:171], v[176:179], v[90:93]
	v_mfma_f32_16x16x32_bf16 v[86:89], v[160:163], v[184:187], v[86:89]
	v_mfma_f32_16x16x32_bf16 v[82:85], v[168:171], v[184:187], v[82:85]
	v_mfma_f32_16x16x32_bf16 v[78:81], v[160:163], v[194:197], v[78:81]
	v_mfma_f32_16x16x32_bf16 v[74:77], v[168:171], v[194:197], v[74:77]
	v_mfma_f32_16x16x32_bf16 v[70:73], v[160:163], v[206:209], v[70:73]
	v_mfma_f32_16x16x32_bf16 v[66:69], v[168:171], v[206:209], v[66:69]
	s_setprio 0
	s_barrier
	ds_read_b128 v[172:175], v137 offset:16384
	ds_read_b128 v[176:179], v137 offset:17408
	ds_read_b128 v[180:183], v137 offset:18432
	ds_read_b128 v[184:187], v137 offset:19456
	ds_read_b128 v[188:191], v137 offset:20480
	ds_read_b128 v[194:197], v137 offset:21504
	ds_read_b128 v[202:205], v137 offset:22528
	ds_read_b128 v[206:209], v137 offset:23552
	s_mov_b32 m0, s41
	s_nop 0
	global_load_lds_dwordx4 v114, s[36:37]
	s_nop 0
	s_mov_b32 m0, s42
	s_nop 0
	global_load_lds_dwordx4 v135, s[36:37]
	s_add_u32 s36, s19, 0x40100
	s_addc_u32 s37, s21, 0
	s_mov_b32 m0, s43
	s_nop 0
	global_load_lds_dwordx4 v114, s[36:37]
	s_nop 0
	s_mov_b32 m0, s44
	s_nop 0
	global_load_lds_dwordx4 v135, s[36:37]
	s_mov_b32 m0, s40
	s_nop 0
	global_load_lds_dwordx4 v65, s[34:35]
	s_nop 0
	s_mov_b32 m0, s45
	s_nop 0
	global_load_lds_dwordx4 v134, s[34:35]
	s_waitcnt vmcnt(8)
	s_waitcnt lgkmcnt(0)
	s_barrier
	s_setprio 1
	s_waitcnt lgkmcnt(0)
	v_mfma_f32_16x16x32_bf16 v[60:63], v[140:143], v[172:175], 0
	v_mfma_f32_16x16x32_bf16 v[56:59], v[148:151], v[172:175], 0
	s_waitcnt lgkmcnt(5)
	v_mfma_f32_16x16x32_bf16 v[52:55], v[140:143], v[180:183], 0
	v_mfma_f32_16x16x32_bf16 v[48:51], v[148:151], v[180:183], 0
	s_waitcnt lgkmcnt(3)
	v_mfma_f32_16x16x32_bf16 v[44:47], v[140:143], v[188:191], 0
	v_mfma_f32_16x16x32_bf16 v[40:43], v[148:151], v[188:191], 0
	s_waitcnt lgkmcnt(1)
	v_mfma_f32_16x16x32_bf16 v[36:39], v[140:143], v[202:205], 0
	v_mfma_f32_16x16x32_bf16 v[32:35], v[148:151], v[202:205], 0
	v_mfma_f32_16x16x32_bf16 v[60:63], v[144:147], v[176:179], v[60:63]
	v_mfma_f32_16x16x32_bf16 v[56:59], v[152:155], v[176:179], v[56:59]
	v_mfma_f32_16x16x32_bf16 v[52:55], v[144:147], v[184:187], v[52:55]
	v_mfma_f32_16x16x32_bf16 v[48:51], v[152:155], v[184:187], v[48:51]
	v_mfma_f32_16x16x32_bf16 v[44:47], v[144:147], v[194:197], v[44:47]
	v_mfma_f32_16x16x32_bf16 v[40:43], v[152:155], v[194:197], v[40:43]
	s_waitcnt lgkmcnt(0)
	v_mfma_f32_16x16x32_bf16 v[36:39], v[144:147], v[206:209], v[36:39]
	v_mfma_f32_16x16x32_bf16 v[32:35], v[152:155], v[206:209], v[32:35]
	s_setprio 0
	s_setprio 1
	v_mfma_f32_16x16x32_bf16 v[28:31], v[156:159], v[172:175], 0
	v_mfma_f32_16x16x32_bf16 v[24:27], v[164:167], v[172:175], 0
	v_mfma_f32_16x16x32_bf16 v[20:23], v[156:159], v[180:183], 0
	v_mfma_f32_16x16x32_bf16 v[16:19], v[164:167], v[180:183], 0
	v_mfma_f32_16x16x32_bf16 v[12:15], v[156:159], v[188:191], 0
	v_mfma_f32_16x16x32_bf16 v[8:11], v[164:167], v[188:191], 0
	v_mfma_f32_16x16x32_bf16 v[4:7], v[156:159], v[202:205], 0
	v_mfma_f32_16x16x32_bf16 v[0:3], v[164:167], v[202:205], 0
	v_mfma_f32_16x16x32_bf16 v[28:31], v[160:163], v[176:179], v[28:31]
	v_mfma_f32_16x16x32_bf16 v[24:27], v[168:171], v[176:179], v[24:27]
	v_mfma_f32_16x16x32_bf16 v[20:23], v[160:163], v[184:187], v[20:23]
	v_mfma_f32_16x16x32_bf16 v[16:19], v[168:171], v[184:187], v[16:19]
	v_mfma_f32_16x16x32_bf16 v[12:15], v[160:163], v[194:197], v[12:15]
	v_mfma_f32_16x16x32_bf16 v[8:11], v[168:171], v[194:197], v[8:11]
	v_mfma_f32_16x16x32_bf16 v[4:7], v[160:163], v[206:209], v[4:7]
	v_mfma_f32_16x16x32_bf16 v[0:3], v[168:171], v[206:209], v[0:3]
	s_setprio 0
	s_barrier
	v_add_u32_e32 v133, 0x18000, v136
	v_add_u32_e32 v139, 0x1c000, v136
	ds_read_b128 v[140:143], v133
	ds_read_b128 v[144:147], v133 offset:1024
	ds_read_b128 v[148:151], v133 offset:2048
	ds_read_b128 v[152:155], v133 offset:3072
	ds_read_b128 v[156:159], v139
	ds_read_b128 v[160:163], v139 offset:1024
	ds_read_b128 v[164:167], v139 offset:2048
	ds_read_b128 v[168:171], v139 offset:3072
	ds_read_b128 v[172:175], v137 offset:32768
	ds_read_b128 v[176:179], v137 offset:33792
	ds_read_b128 v[180:183], v137 offset:34816
	ds_read_b128 v[184:187], v137 offset:35840
	ds_read_b128 v[188:191], v137 offset:36864
	ds_read_b128 v[194:197], v137 offset:37888
	ds_read_b128 v[202:205], v137 offset:38912
	ds_read_b128 v[206:209], v137 offset:39936
	s_add_u32 s34, s33, 0x40100
	s_addc_u32 s35, s61, 0
	s_mov_b32 m0, s46
	s_nop 0
	global_load_lds_dwordx4 v65, s[34:35]
	s_nop 0
	s_mov_b32 m0, s47
	s_nop 0
	global_load_lds_dwordx4 v134, s[34:35]
	s_waitcnt vmcnt(8)
	s_waitcnt lgkmcnt(0)
	s_barrier
	s_setprio 1
	s_waitcnt lgkmcnt(0)
	v_mfma_f32_16x16x32_bf16 v[128:131], v[140:143], v[172:175], v[128:131]
	v_mfma_f32_16x16x32_bf16 v[124:127], v[148:151], v[172:175], v[124:127]
	s_waitcnt lgkmcnt(5)
	v_mfma_f32_16x16x32_bf16 v[120:123], v[140:143], v[180:183], v[120:123]
	v_mfma_f32_16x16x32_bf16 v[116:119], v[148:151], v[180:183], v[116:119]
	s_waitcnt lgkmcnt(3)
	v_mfma_f32_16x16x32_bf16 v[110:113], v[140:143], v[188:191], v[110:113]
	v_mfma_f32_16x16x32_bf16 v[106:109], v[148:151], v[188:191], v[106:109]
	s_waitcnt lgkmcnt(1)
	v_mfma_f32_16x16x32_bf16 v[102:105], v[140:143], v[202:205], v[102:105]
	v_mfma_f32_16x16x32_bf16 v[98:101], v[148:151], v[202:205], v[98:101]
	v_mfma_f32_16x16x32_bf16 v[128:131], v[144:147], v[176:179], v[128:131]
	v_mfma_f32_16x16x32_bf16 v[124:127], v[152:155], v[176:179], v[124:127]
	v_mfma_f32_16x16x32_bf16 v[120:123], v[144:147], v[184:187], v[120:123]
	v_mfma_f32_16x16x32_bf16 v[116:119], v[152:155], v[184:187], v[116:119]
	v_mfma_f32_16x16x32_bf16 v[110:113], v[144:147], v[194:197], v[110:113]
	v_mfma_f32_16x16x32_bf16 v[106:109], v[152:155], v[194:197], v[106:109]
	s_waitcnt lgkmcnt(0)
	v_mfma_f32_16x16x32_bf16 v[102:105], v[144:147], v[206:209], v[102:105]
	v_mfma_f32_16x16x32_bf16 v[98:101], v[152:155], v[206:209], v[98:101]
	s_setprio 0
	s_setprio 1
	v_mfma_f32_16x16x32_bf16 v[94:97], v[156:159], v[172:175], v[94:97]
	v_mfma_f32_16x16x32_bf16 v[90:93], v[164:167], v[172:175], v[90:93]
	v_mfma_f32_16x16x32_bf16 v[86:89], v[156:159], v[180:183], v[86:89]
	v_mfma_f32_16x16x32_bf16 v[82:85], v[164:167], v[180:183], v[82:85]
	v_mfma_f32_16x16x32_bf16 v[78:81], v[156:159], v[188:191], v[78:81]
	v_mfma_f32_16x16x32_bf16 v[74:77], v[164:167], v[188:191], v[74:77]
	v_mfma_f32_16x16x32_bf16 v[70:73], v[156:159], v[202:205], v[70:73]
	v_mfma_f32_16x16x32_bf16 v[66:69], v[164:167], v[202:205], v[66:69]
	v_mfma_f32_16x16x32_bf16 v[94:97], v[160:163], v[176:179], v[94:97]
	v_mfma_f32_16x16x32_bf16 v[90:93], v[168:171], v[176:179], v[90:93]
	v_mfma_f32_16x16x32_bf16 v[86:89], v[160:163], v[184:187], v[86:89]
	v_mfma_f32_16x16x32_bf16 v[82:85], v[168:171], v[184:187], v[82:85]
	v_mfma_f32_16x16x32_bf16 v[78:81], v[160:163], v[194:197], v[78:81]
	v_mfma_f32_16x16x32_bf16 v[74:77], v[168:171], v[194:197], v[74:77]
	v_mfma_f32_16x16x32_bf16 v[70:73], v[160:163], v[206:209], v[70:73]
	v_mfma_f32_16x16x32_bf16 v[66:69], v[168:171], v[206:209], v[66:69]
	s_setprio 0
	s_barrier
	ds_read_b128 v[172:175], v137 offset:49152
	ds_read_b128 v[176:179], v137 offset:50176
	ds_read_b128 v[180:183], v137 offset:51200
	ds_read_b128 v[184:187], v137 offset:52224
	ds_read_b128 v[188:191], v137 offset:53248
	ds_read_b128 v[194:197], v137 offset:54272
	ds_read_b128 v[202:205], v137 offset:55296
	ds_read_b128 v[206:209], v137 offset:56320
	s_add_u32 s34, s19, 0x180
	s_addc_u32 s35, s21, 0
	s_mov_b32 m0, s51
	s_nop 0
	global_load_lds_dwordx4 v114, s[34:35]
	s_nop 0
	s_mov_b32 m0, s52
	s_nop 0
	global_load_lds_dwordx4 v135, s[34:35]
	s_add_u32 s34, s19, 0x40180
	s_addc_u32 s35, s21, 0
	s_mov_b32 m0, s55
	s_nop 0
	global_load_lds_dwordx4 v114, s[34:35]
	s_nop 0
	s_mov_b32 m0, s56
	s_nop 0
	global_load_lds_dwordx4 v135, s[34:35]
	s_nop 0
	s_mov_b32 m0, s53
	s_nop 0
	global_load_lds_dwordx4 v65, s[26:27]
	s_nop 0
	s_mov_b32 m0, s54
	s_nop 0
	global_load_lds_dwordx4 v134, s[26:27]
	s_waitcnt vmcnt(8)
	s_waitcnt lgkmcnt(0)
	s_barrier
	s_setprio 1
	s_waitcnt lgkmcnt(0)
	v_mfma_f32_16x16x32_bf16 v[60:63], v[140:143], v[172:175], v[60:63]
	v_mfma_f32_16x16x32_bf16 v[56:59], v[148:151], v[172:175], v[56:59]
	s_waitcnt lgkmcnt(5)
	v_mfma_f32_16x16x32_bf16 v[52:55], v[140:143], v[180:183], v[52:55]
	v_mfma_f32_16x16x32_bf16 v[48:51], v[148:151], v[180:183], v[48:51]
	s_waitcnt lgkmcnt(3)
	v_mfma_f32_16x16x32_bf16 v[44:47], v[140:143], v[188:191], v[44:47]
	v_mfma_f32_16x16x32_bf16 v[40:43], v[148:151], v[188:191], v[40:43]
	s_waitcnt lgkmcnt(1)
	v_mfma_f32_16x16x32_bf16 v[36:39], v[140:143], v[202:205], v[36:39]
	v_mfma_f32_16x16x32_bf16 v[32:35], v[148:151], v[202:205], v[32:35]
	v_mfma_f32_16x16x32_bf16 v[60:63], v[144:147], v[176:179], v[60:63]
	v_mfma_f32_16x16x32_bf16 v[56:59], v[152:155], v[176:179], v[56:59]
	v_mfma_f32_16x16x32_bf16 v[52:55], v[144:147], v[184:187], v[52:55]
	v_mfma_f32_16x16x32_bf16 v[48:51], v[152:155], v[184:187], v[48:51]
	v_mfma_f32_16x16x32_bf16 v[44:47], v[144:147], v[194:197], v[44:47]
	v_mfma_f32_16x16x32_bf16 v[40:43], v[152:155], v[194:197], v[40:43]
	s_waitcnt lgkmcnt(0)
	v_mfma_f32_16x16x32_bf16 v[36:39], v[144:147], v[206:209], v[36:39]
	v_mfma_f32_16x16x32_bf16 v[32:35], v[152:155], v[206:209], v[32:35]
	s_setprio 0
	s_setprio 1
	v_mfma_f32_16x16x32_bf16 v[28:31], v[156:159], v[172:175], v[28:31]
	v_mfma_f32_16x16x32_bf16 v[24:27], v[164:167], v[172:175], v[24:27]
	v_mfma_f32_16x16x32_bf16 v[20:23], v[156:159], v[180:183], v[20:23]
	v_mfma_f32_16x16x32_bf16 v[16:19], v[164:167], v[180:183], v[16:19]
	v_mfma_f32_16x16x32_bf16 v[12:15], v[156:159], v[188:191], v[12:15]
	v_mfma_f32_16x16x32_bf16 v[8:11], v[164:167], v[188:191], v[8:11]
	v_mfma_f32_16x16x32_bf16 v[4:7], v[156:159], v[202:205], v[4:7]
	v_mfma_f32_16x16x32_bf16 v[0:3], v[164:167], v[202:205], v[0:3]
	v_mfma_f32_16x16x32_bf16 v[28:31], v[160:163], v[176:179], v[28:31]
	v_mfma_f32_16x16x32_bf16 v[24:27], v[168:171], v[176:179], v[24:27]
	v_mfma_f32_16x16x32_bf16 v[20:23], v[160:163], v[184:187], v[20:23]
	v_mfma_f32_16x16x32_bf16 v[16:19], v[168:171], v[184:187], v[16:19]
	v_mfma_f32_16x16x32_bf16 v[12:15], v[160:163], v[194:197], v[12:15]
	v_mfma_f32_16x16x32_bf16 v[8:11], v[168:171], v[194:197], v[8:11]
	v_mfma_f32_16x16x32_bf16 v[4:7], v[160:163], v[206:209], v[4:7]
	v_mfma_f32_16x16x32_bf16 v[0:3], v[168:171], v[206:209], v[0:3]
	s_setprio 0
	s_barrier
	s_add_i32 s17, s17, 2
	s_add_u32 s2, s2, 0x100
	s_addc_u32 s3, s3, 0
	s_cmp_lt_u32 s17, 12

.LBB0_624:
	v_add_u32_e32 v114, 0x10000, v143
	v_add_u32_e32 v133, 0x14000, v143
	ds_read_b128 v[134:137], v114
	ds_read_b128 v[146:149], v114 offset:1024
	ds_read_b128 v[150:153], v114 offset:2048
	ds_read_b128 v[154:157], v114 offset:3072
	ds_read_b128 v[158:161], v133
	ds_read_b128 v[162:165], v133 offset:1024
	ds_read_b128 v[166:169], v133 offset:2048
	ds_read_b128 v[170:173], v133 offset:3072
	ds_read_b128 v[174:177], v144
	ds_read_b128 v[178:181], v144 offset:1024
	ds_read_b128 v[182:185], v144 offset:2048
	ds_read_b128 v[186:189], v144 offset:3072
	ds_read_b128 v[202:205], v144 offset:4096
	ds_read_b128 v[206:209], v144 offset:5120
	ds_read_b128 v[210:213], v144 offset:6144
	ds_read_b128 v[214:217], v144 offset:7168
	s_add_i32 s63, s63, 1
	v_readlane_b32 s2, v254, 38
	s_mul_i32 s2, s63, s2
	s_mul_hi_u32 s3, s63, s70
	s_add_i32 s3, s3, s2
	s_mul_i32 s2, s63, s70
	v_readlane_b32 s13, v255, 0
	s_add_u32 s2, s2, s13
	s_addc_u32 s3, s3, s62
	v_mov_b64_e32 v[0:1], 0x4c8
	v_cmp_lt_i64_e64 s[34:35], s[2:3], v[0:1]
	v_mov_b64_e32 v[0:1], 0x4c7
	v_cmp_gt_i64_e32 vcc, s[2:3], v[0:1]
	s_nop 3
	s_cmp_lg_u64 s[34:35], 0
	s_cselect_b64 s[100:101], -1, 1
	s_cbranch_vccnz .LBB0_626
	s_ashr_i32 s3, s2, 31
	s_lshr_b32 s3, s3, 29
	s_add_i32 s3, s2, s3
	s_ashr_i32 s12, s3, 3
	s_and_b32 s3, s3, -8
	s_sub_i32 s2, s2, s3
	s_cmp_lt_i32 s2, 0
	s_movk_i32 s3, 0x9a
	s_cselect_b32 s3, s3, 0x99
	s_mul_i32 s2, s2, s3
	s_add_i32 s2, s2, s12
	s_mul_hi_i32 s3, s2, 0x38e38e39
	s_lshr_b32 s12, s3, 31
	s_ashr_i32 s3, s3, 4
	s_add_i32 s3, s3, s12
	s_lshl_b32 s13, s3, 3
	s_sub_i32 s12, 0x88, s13
	s_min_i32 s14, s12, 8
	s_abs_i32 s12, s14
	v_cvt_f32_u32_e32 v0, s12
	s_sub_i32 s16, 0, s12
	s_mulk_i32 s3, 0x48
	s_sub_i32 s2, s2, s3
	v_rcp_iflag_f32_e32 v0, v0
	s_abs_i32 s3, s2
	s_xor_b32 s15, s2, s14
	s_ashr_i32 s15, s15, 31
	v_mul_f32_e32 v0, 0x4f7ffffe, v0
	v_cvt_u32_f32_e32 v0, v0
	s_nop 0
	v_readfirstlane_b32 s17, v0
	s_mul_i32 s16, s16, s17
	s_mul_hi_u32 s16, s17, s16
	s_add_i32 s17, s17, s16
	s_mul_hi_u32 s16, s3, s17
	s_mul_i32 s17, s16, s12
	s_sub_i32 s3, s3, s17
	s_add_i32 s18, s16, 1
	s_sub_i32 s17, s3, s12
	s_cmp_ge_u32 s3, s12
	s_cselect_b32 s16, s18, s16
	s_cselect_b32 s3, s17, s3
	s_add_i32 s17, s16, 1
	s_cmp_ge_u32 s3, s12
	s_cselect_b32 s3, s17, s16
	s_xor_b32 s3, s3, s15
	s_sub_i32 s12, s3, s15
	s_mul_i32 s3, s12, s14
	s_sub_i32 s2, s2, s3
	s_add_i32 s14, s13, s2
.LBB0_626:
	v_mov_b32_e32 v0, 0
	s_mov_b32 s13, -2
	s_mov_b64 s[2:3], 0
	v_mov_b32_e32 v1, v0
	s_waitcnt lgkmcnt(0)
	s_add_u32 s33, s24, s2
	s_addc_u32 s40, s25, s3
	s_add_u32 s18, s33, 0x100
	s_addc_u32 s19, s40, 0
	s_add_u32 s16, s33, 0x180
	s_addc_u32 s17, s40, 0
	s_add_u32 s15, s26, s2
	s_addc_u32 s23, s27, s3
	s_add_u32 s36, s15, 0x100
	s_addc_u32 s37, s23, 0
	s_add_u32 s38, s33, 0x40080
	s_addc_u32 s39, s40, 0
	s_mov_b32 m0, s60
	s_nop 0
	global_load_lds_dwordx4 v65, s[38:39]
	s_nop 0
	s_mov_b32 m0, s61
	s_nop 0
	global_load_lds_dwordx4 v141, s[38:39]
	s_waitcnt vmcnt(8)
	s_waitcnt lgkmcnt(0)
	s_barrier
	s_setprio 1
	s_waitcnt lgkmcnt(0)
	v_mfma_f32_16x16x32_bf16 v[128:131], v[134:137], v[174:177], 0
	v_mfma_f32_16x16x32_bf16 v[124:127], v[150:153], v[174:177], 0
	v_mfma_f32_16x16x32_bf16 v[120:123], v[134:137], v[182:185], 0
	v_mfma_f32_16x16x32_bf16 v[116:119], v[150:153], v[182:185], 0
	v_mfma_f32_16x16x32_bf16 v[110:113], v[134:137], v[202:205], 0
	v_mfma_f32_16x16x32_bf16 v[106:109], v[150:153], v[202:205], 0
	v_mfma_f32_16x16x32_bf16 v[102:105], v[134:137], v[210:213], 0
	v_mfma_f32_16x16x32_bf16 v[98:101], v[150:153], v[210:213], 0
	v_mfma_f32_16x16x32_bf16 v[128:131], v[146:149], v[178:181], v[128:131]
	v_mfma_f32_16x16x32_bf16 v[124:127], v[154:157], v[178:181], v[124:127]
	v_mfma_f32_16x16x32_bf16 v[120:123], v[146:149], v[186:189], v[120:123]
	v_mfma_f32_16x16x32_bf16 v[116:119], v[154:157], v[186:189], v[116:119]
	v_mfma_f32_16x16x32_bf16 v[110:113], v[146:149], v[206:209], v[110:113]
	v_mfma_f32_16x16x32_bf16 v[106:109], v[154:157], v[206:209], v[106:109]
	v_mfma_f32_16x16x32_bf16 v[102:105], v[146:149], v[214:217], v[102:105]
	v_mfma_f32_16x16x32_bf16 v[98:101], v[154:157], v[214:217], v[98:101]
	s_setprio 0
	s_setprio 1
	v_mfma_f32_16x16x32_bf16 v[94:97], v[158:161], v[174:177], 0
	v_mfma_f32_16x16x32_bf16 v[90:93], v[166:169], v[174:177], 0
	v_mfma_f32_16x16x32_bf16 v[86:89], v[158:161], v[182:185], 0
	v_mfma_f32_16x16x32_bf16 v[82:85], v[166:169], v[182:185], 0
	v_mfma_f32_16x16x32_bf16 v[78:81], v[158:161], v[202:205], 0
	v_mfma_f32_16x16x32_bf16 v[74:77], v[166:169], v[202:205], 0
	v_mfma_f32_16x16x32_bf16 v[70:73], v[158:161], v[210:213], 0
	v_mfma_f32_16x16x32_bf16 v[66:69], v[166:169], v[210:213], 0
	v_mfma_f32_16x16x32_bf16 v[94:97], v[162:165], v[178:181], v[94:97]
	v_mfma_f32_16x16x32_bf16 v[90:93], v[170:173], v[178:181], v[90:93]
	v_mfma_f32_16x16x32_bf16 v[86:89], v[162:165], v[186:189], v[86:89]
	v_mfma_f32_16x16x32_bf16 v[82:85], v[170:173], v[186:189], v[82:85]
	v_mfma_f32_16x16x32_bf16 v[78:81], v[162:165], v[206:209], v[78:81]
	v_mfma_f32_16x16x32_bf16 v[74:77], v[170:173], v[206:209], v[74:77]
	v_mfma_f32_16x16x32_bf16 v[70:73], v[162:165], v[214:217], v[70:73]
	v_mfma_f32_16x16x32_bf16 v[66:69], v[170:173], v[214:217], v[66:69]
	s_setprio 0
	s_barrier
	ds_read_b128 v[174:177], v144 offset:16384
	ds_read_b128 v[178:181], v144 offset:17408
	ds_read_b128 v[182:185], v144 offset:18432
	ds_read_b128 v[186:189], v144 offset:19456
	ds_read_b128 v[202:205], v144 offset:20480
	ds_read_b128 v[206:209], v144 offset:21504
	ds_read_b128 v[210:213], v144 offset:22528
	ds_read_b128 v[214:217], v144 offset:23552
	s_mov_b32 m0, s48
	s_nop 0
	global_load_lds_dwordx4 v140, s[36:37]
	s_nop 0
	s_mov_b32 m0, s49
	s_nop 0
	global_load_lds_dwordx4 v142, s[36:37]
	s_add_u32 s36, s15, 0x40100
	s_addc_u32 s37, s23, 0
	s_mov_b32 m0, s50
	s_nop 0
	global_load_lds_dwordx4 v140, s[36:37]
	s_nop 0
	s_mov_b32 m0, s51
	s_nop 0
	global_load_lds_dwordx4 v142, s[36:37]
	s_mov_b32 m0, s47
	s_nop 0
	global_load_lds_dwordx4 v65, s[18:19]
	s_nop 0
	s_mov_b32 m0, s52
	s_nop 0
	global_load_lds_dwordx4 v141, s[18:19]
	s_waitcnt vmcnt(8)
	s_waitcnt lgkmcnt(0)
	s_barrier
	s_setprio 1
	s_waitcnt lgkmcnt(0)
	v_mfma_f32_16x16x32_bf16 v[60:63], v[134:137], v[174:177], 0
	v_mfma_f32_16x16x32_bf16 v[56:59], v[150:153], v[174:177], 0
	s_waitcnt lgkmcnt(5)
	v_mfma_f32_16x16x32_bf16 v[52:55], v[134:137], v[182:185], 0
	v_mfma_f32_16x16x32_bf16 v[48:51], v[150:153], v[182:185], 0
	s_waitcnt lgkmcnt(3)
	v_mfma_f32_16x16x32_bf16 v[44:47], v[134:137], v[202:205], 0
	v_mfma_f32_16x16x32_bf16 v[40:43], v[150:153], v[202:205], 0
	s_waitcnt lgkmcnt(1)
	v_mfma_f32_16x16x32_bf16 v[36:39], v[134:137], v[210:213], 0
	v_mfma_f32_16x16x32_bf16 v[32:35], v[150:153], v[210:213], 0
	v_mfma_f32_16x16x32_bf16 v[60:63], v[146:149], v[178:181], v[60:63]
	v_mfma_f32_16x16x32_bf16 v[56:59], v[154:157], v[178:181], v[56:59]
	v_mfma_f32_16x16x32_bf16 v[52:55], v[146:149], v[186:189], v[52:55]
	v_mfma_f32_16x16x32_bf16 v[48:51], v[154:157], v[186:189], v[48:51]
	v_mfma_f32_16x16x32_bf16 v[44:47], v[146:149], v[206:209], v[44:47]
	v_mfma_f32_16x16x32_bf16 v[40:43], v[154:157], v[206:209], v[40:43]
	s_waitcnt lgkmcnt(0)
	v_mfma_f32_16x16x32_bf16 v[36:39], v[146:149], v[214:217], v[36:39]
	v_mfma_f32_16x16x32_bf16 v[32:35], v[154:157], v[214:217], v[32:35]
	s_setprio 0
	s_setprio 1
	v_mfma_f32_16x16x32_bf16 v[28:31], v[158:161], v[174:177], 0
	v_mfma_f32_16x16x32_bf16 v[24:27], v[166:169], v[174:177], 0
	v_mfma_f32_16x16x32_bf16 v[20:23], v[158:161], v[182:185], 0
	v_mfma_f32_16x16x32_bf16 v[16:19], v[166:169], v[182:185], 0
	v_mfma_f32_16x16x32_bf16 v[12:15], v[158:161], v[202:205], 0
	v_mfma_f32_16x16x32_bf16 v[8:11], v[166:169], v[202:205], 0
	v_mfma_f32_16x16x32_bf16 v[4:7], v[158:161], v[210:213], 0
	v_mfma_f32_16x16x32_bf16 v[0:3], v[166:169], v[210:213], 0
	v_mfma_f32_16x16x32_bf16 v[28:31], v[162:165], v[178:181], v[28:31]
	v_mfma_f32_16x16x32_bf16 v[24:27], v[170:173], v[178:181], v[24:27]
	v_mfma_f32_16x16x32_bf16 v[20:23], v[162:165], v[186:189], v[20:23]
	v_mfma_f32_16x16x32_bf16 v[16:19], v[170:173], v[186:189], v[16:19]
	v_mfma_f32_16x16x32_bf16 v[12:15], v[162:165], v[206:209], v[12:15]
	v_mfma_f32_16x16x32_bf16 v[8:11], v[170:173], v[206:209], v[8:11]
	v_mfma_f32_16x16x32_bf16 v[4:7], v[162:165], v[214:217], v[4:7]
	v_mfma_f32_16x16x32_bf16 v[0:3], v[170:173], v[214:217], v[0:3]
	s_setprio 0
	s_barrier
	v_add_u32_e32 v132, 0x18000, v143
	v_add_u32_e32 v134, 0x1c000, v143
	ds_read_b128 v[136:139], v132
	ds_read_b128 v[146:149], v132 offset:1024
	ds_read_b128 v[150:153], v132 offset:2048
	ds_read_b128 v[154:157], v132 offset:3072
	ds_read_b128 v[158:161], v134
	ds_read_b128 v[162:165], v134 offset:1024
	ds_read_b128 v[166:169], v134 offset:2048
	ds_read_b128 v[170:173], v134 offset:3072
	ds_read_b128 v[174:177], v144 offset:32768
	ds_read_b128 v[178:181], v144 offset:33792
	ds_read_b128 v[182:185], v144 offset:34816
	ds_read_b128 v[186:189], v144 offset:35840
	ds_read_b128 v[202:205], v144 offset:36864
	ds_read_b128 v[206:209], v144 offset:37888
	ds_read_b128 v[210:213], v144 offset:38912
	ds_read_b128 v[214:217], v144 offset:39936
	s_add_u32 s18, s33, 0x40100
	s_addc_u32 s19, s40, 0
	s_mov_b32 m0, s53
	s_nop 0
	global_load_lds_dwordx4 v65, s[18:19]
	s_nop 0
	s_mov_b32 m0, s54
	s_nop 0
	global_load_lds_dwordx4 v141, s[18:19]
	s_waitcnt vmcnt(8)
	s_waitcnt lgkmcnt(0)
	s_barrier
	s_setprio 1
	s_waitcnt lgkmcnt(0)
	v_mfma_f32_16x16x32_bf16 v[128:131], v[136:139], v[174:177], v[128:131]
	v_mfma_f32_16x16x32_bf16 v[124:127], v[150:153], v[174:177], v[124:127]
	s_waitcnt lgkmcnt(5)
	v_mfma_f32_16x16x32_bf16 v[120:123], v[136:139], v[182:185], v[120:123]
	v_mfma_f32_16x16x32_bf16 v[116:119], v[150:153], v[182:185], v[116:119]
	s_waitcnt lgkmcnt(3)
	v_mfma_f32_16x16x32_bf16 v[110:113], v[136:139], v[202:205], v[110:113]
	v_mfma_f32_16x16x32_bf16 v[106:109], v[150:153], v[202:205], v[106:109]
	s_waitcnt lgkmcnt(1)
	v_mfma_f32_16x16x32_bf16 v[102:105], v[136:139], v[210:213], v[102:105]
	v_mfma_f32_16x16x32_bf16 v[98:101], v[150:153], v[210:213], v[98:101]
	v_mfma_f32_16x16x32_bf16 v[128:131], v[146:149], v[178:181], v[128:131]
	v_mfma_f32_16x16x32_bf16 v[124:127], v[154:157], v[178:181], v[124:127]
	v_mfma_f32_16x16x32_bf16 v[120:123], v[146:149], v[186:189], v[120:123]
	v_mfma_f32_16x16x32_bf16 v[116:119], v[154:157], v[186:189], v[116:119]
	v_mfma_f32_16x16x32_bf16 v[110:113], v[146:149], v[206:209], v[110:113]
	v_mfma_f32_16x16x32_bf16 v[106:109], v[154:157], v[206:209], v[106:109]
	s_waitcnt lgkmcnt(0)
	v_mfma_f32_16x16x32_bf16 v[102:105], v[146:149], v[214:217], v[102:105]
	v_mfma_f32_16x16x32_bf16 v[98:101], v[154:157], v[214:217], v[98:101]
	s_setprio 0
	s_setprio 1
	v_mfma_f32_16x16x32_bf16 v[94:97], v[158:161], v[174:177], v[94:97]
	v_mfma_f32_16x16x32_bf16 v[90:93], v[166:169], v[174:177], v[90:93]
	v_mfma_f32_16x16x32_bf16 v[86:89], v[158:161], v[182:185], v[86:89]
	v_mfma_f32_16x16x32_bf16 v[82:85], v[166:169], v[182:185], v[82:85]
	v_mfma_f32_16x16x32_bf16 v[78:81], v[158:161], v[202:205], v[78:81]
	v_mfma_f32_16x16x32_bf16 v[74:77], v[166:169], v[202:205], v[74:77]
	v_mfma_f32_16x16x32_bf16 v[70:73], v[158:161], v[210:213], v[70:73]
	v_mfma_f32_16x16x32_bf16 v[66:69], v[166:169], v[210:213], v[66:69]
	v_mfma_f32_16x16x32_bf16 v[94:97], v[162:165], v[178:181], v[94:97]
	v_mfma_f32_16x16x32_bf16 v[90:93], v[170:173], v[178:181], v[90:93]
	v_mfma_f32_16x16x32_bf16 v[86:89], v[162:165], v[186:189], v[86:89]
	v_mfma_f32_16x16x32_bf16 v[82:85], v[170:173], v[186:189], v[82:85]
	v_mfma_f32_16x16x32_bf16 v[78:81], v[162:165], v[206:209], v[78:81]
	v_mfma_f32_16x16x32_bf16 v[74:77], v[170:173], v[206:209], v[74:77]
	v_mfma_f32_16x16x32_bf16 v[70:73], v[162:165], v[214:217], v[70:73]
	v_mfma_f32_16x16x32_bf16 v[66:69], v[170:173], v[214:217], v[66:69]
	s_setprio 0
	s_barrier
	ds_read_b128 v[174:177], v144 offset:49152
	ds_read_b128 v[178:181], v144 offset:50176
	ds_read_b128 v[182:185], v144 offset:51200
	ds_read_b128 v[186:189], v144 offset:52224
	ds_read_b128 v[202:205], v144 offset:53248
	ds_read_b128 v[206:209], v144 offset:54272
	ds_read_b128 v[210:213], v144 offset:55296
	ds_read_b128 v[214:217], v144 offset:56320
	s_add_u32 s18, s15, 0x180
	s_addc_u32 s19, s23, 0
	s_mov_b32 m0, s30
	s_nop 0
	global_load_lds_dwordx4 v140, s[18:19]
	s_nop 0
	s_mov_b32 m0, s55
	s_nop 0
	global_load_lds_dwordx4 v142, s[18:19]
	s_add_u32 s18, s15, 0x40180
	s_addc_u32 s19, s23, 0
	s_mov_b32 m0, s58
	s_nop 0
	global_load_lds_dwordx4 v140, s[18:19]
	s_nop 0
	s_mov_b32 m0, s59
	s_nop 0
	global_load_lds_dwordx4 v142, s[18:19]
	s_nop 0
	s_mov_b32 m0, s56
	s_nop 0
	global_load_lds_dwordx4 v65, s[16:17]
	s_nop 0
	s_mov_b32 m0, s57
	s_nop 0
	global_load_lds_dwordx4 v141, s[16:17]
	s_waitcnt vmcnt(8)
	s_waitcnt lgkmcnt(0)
	s_barrier
	s_setprio 1
	s_waitcnt lgkmcnt(0)
	v_mfma_f32_16x16x32_bf16 v[60:63], v[136:139], v[174:177], v[60:63]
	v_mfma_f32_16x16x32_bf16 v[56:59], v[150:153], v[174:177], v[56:59]
	s_waitcnt lgkmcnt(5)
	v_mfma_f32_16x16x32_bf16 v[52:55], v[136:139], v[182:185], v[52:55]
	v_mfma_f32_16x16x32_bf16 v[48:51], v[150:153], v[182:185], v[48:51]
	s_waitcnt lgkmcnt(3)
	v_mfma_f32_16x16x32_bf16 v[44:47], v[136:139], v[202:205], v[44:47]
	v_mfma_f32_16x16x32_bf16 v[40:43], v[150:153], v[202:205], v[40:43]
	s_waitcnt lgkmcnt(1)
	v_mfma_f32_16x16x32_bf16 v[36:39], v[136:139], v[210:213], v[36:39]
	v_mfma_f32_16x16x32_bf16 v[32:35], v[150:153], v[210:213], v[32:35]
	v_mfma_f32_16x16x32_bf16 v[60:63], v[146:149], v[178:181], v[60:63]
	v_mfma_f32_16x16x32_bf16 v[56:59], v[154:157], v[178:181], v[56:59]
	v_mfma_f32_16x16x32_bf16 v[52:55], v[146:149], v[186:189], v[52:55]
	v_mfma_f32_16x16x32_bf16 v[48:51], v[154:157], v[186:189], v[48:51]
	v_mfma_f32_16x16x32_bf16 v[44:47], v[146:149], v[206:209], v[44:47]
	v_mfma_f32_16x16x32_bf16 v[40:43], v[154:157], v[206:209], v[40:43]
	s_waitcnt lgkmcnt(0)
	v_mfma_f32_16x16x32_bf16 v[36:39], v[146:149], v[214:217], v[36:39]
	v_mfma_f32_16x16x32_bf16 v[32:35], v[154:157], v[214:217], v[32:35]
	s_setprio 0
	s_setprio 1
	v_mfma_f32_16x16x32_bf16 v[28:31], v[158:161], v[174:177], v[28:31]
	v_mfma_f32_16x16x32_bf16 v[24:27], v[166:169], v[174:177], v[24:27]
	v_mfma_f32_16x16x32_bf16 v[20:23], v[158:161], v[182:185], v[20:23]
	v_mfma_f32_16x16x32_bf16 v[16:19], v[166:169], v[182:185], v[16:19]
	v_mfma_f32_16x16x32_bf16 v[12:15], v[158:161], v[202:205], v[12:15]
	v_mfma_f32_16x16x32_bf16 v[8:11], v[166:169], v[202:205], v[8:11]
	v_mfma_f32_16x16x32_bf16 v[4:7], v[158:161], v[210:213], v[4:7]
	v_mfma_f32_16x16x32_bf16 v[0:3], v[166:169], v[210:213], v[0:3]
	v_mfma_f32_16x16x32_bf16 v[28:31], v[162:165], v[178:181], v[28:31]
	v_mfma_f32_16x16x32_bf16 v[24:27], v[170:173], v[178:181], v[24:27]
	v_mfma_f32_16x16x32_bf16 v[20:23], v[162:165], v[186:189], v[20:23]
	v_mfma_f32_16x16x32_bf16 v[16:19], v[170:173], v[186:189], v[16:19]
	v_mfma_f32_16x16x32_bf16 v[12:15], v[162:165], v[206:209], v[12:15]
	v_mfma_f32_16x16x32_bf16 v[8:11], v[170:173], v[206:209], v[8:11]
	v_mfma_f32_16x16x32_bf16 v[4:7], v[162:165], v[214:217], v[4:7]
	v_mfma_f32_16x16x32_bf16 v[0:3], v[170:173], v[214:217], v[0:3]
	s_setprio 0
	s_barrier
	s_add_i32 s13, s13, 2
	s_add_u32 s2, s2, 0x100
	s_addc_u32 s3, s3, 0
	s_cmp_lt_u32 s13, 12

.LBB0_1108:
	v_add_u32_e32 v132, 0x10000, v204
	v_add_u32_e32 v134, 0x14000, v204
	ds_read_b128 v[136:139], v132
	ds_read_b128 v[140:143], v132 offset:1024
	ds_read_b128 v[144:147], v132 offset:2048
	ds_read_b128 v[148:151], v132 offset:3072
	ds_read_b128 v[152:155], v134
	ds_read_b128 v[156:159], v134 offset:1024
	ds_read_b128 v[160:163], v134 offset:2048
	ds_read_b128 v[164:167], v134 offset:3072
	ds_read_b128 v[168:171], v205
	ds_read_b128 v[172:175], v205 offset:1024
	ds_read_b128 v[176:179], v205 offset:2048
	ds_read_b128 v[180:183], v205 offset:3072
	ds_read_b128 v[184:187], v205 offset:4096
	ds_read_b128 v[188:191], v205 offset:5120
	ds_read_b128 v[194:197], v205 offset:6144
	ds_read_b128 v[198:201], v205 offset:7168
	s_add_i32 s53, s53, 1
	v_readlane_b32 s0, v254, 38
	s_mul_i32 s0, s53, s0
	s_mul_hi_u32 s1, s53, s70
	s_add_i32 s1, s1, s0
	s_mul_i32 s0, s53, s70
	v_readlane_b32 s2, v255, 0
	s_add_u32 s2, s0, s2
	s_addc_u32 s3, s1, s41
	v_mov_b64_e32 v[0:1], s[30:31]
	v_cmp_ge_i64_e32 vcc, s[2:3], v[0:1]
	v_cmp_lt_i64_e64 s[0:1], s[2:3], v[0:1]
	s_nop 3
	s_cmp_lg_u64 s[0:1], 0
	s_cselect_b64 s[100:101], -1, 1
	s_cbranch_vccnz .LBB0_1110
	s_ashr_i32 s3, s2, 31
	s_lshr_b32 s3, s3, 29
	s_add_i32 s3, s2, s3
	s_ashr_i32 s14, s3, 3
	s_and_b32 s3, s3, -8
	s_sub_i32 s2, s2, s3
	s_cmp_lt_i32 s2, 0
	s_cselect_b32 s3, s42, s40
	s_mul_i32 s2, s3, s2
	s_add_i32 s2, s2, s14
	s_ashr_i32 s3, s2, 31
	s_lshr_b32 s3, s3, 27
	s_add_i32 s3, s2, s3
	s_ashr_i32 s14, s3, 5
	s_lshl_b32 s15, s14, 3
	s_sub_i32 s14, s39, s15
	s_min_i32 s16, s14, 8
	s_abs_i32 s14, s16
	v_cvt_f32_u32_e32 v0, s14
	s_sub_i32 s18, 0, s14
	s_andn2_b32 s3, s3, 31
	s_sub_i32 s2, s2, s3
	v_rcp_iflag_f32_e32 v0, v0
	s_abs_i32 s3, s2
	s_xor_b32 s17, s2, s16
	s_ashr_i32 s17, s17, 31
	v_mul_f32_e32 v0, 0x4f7ffffe, v0
	v_cvt_u32_f32_e32 v0, v0
	s_nop 0
	v_readfirstlane_b32 s19, v0
	s_mul_i32 s18, s18, s19
	s_mul_hi_u32 s18, s19, s18
	s_add_i32 s19, s19, s18
	s_mul_hi_u32 s18, s3, s19
	s_mul_i32 s19, s18, s14
	s_sub_i32 s3, s3, s19
	s_add_i32 s20, s18, 1
	s_sub_i32 s19, s3, s14
	s_cmp_ge_u32 s3, s14
	s_cselect_b32 s18, s20, s18
	s_cselect_b32 s3, s19, s3
	s_add_i32 s19, s18, 1
	s_cmp_ge_u32 s3, s14
	s_cselect_b32 s3, s19, s18
	s_xor_b32 s3, s3, s17
	s_sub_i32 s14, s3, s17
	s_mul_i32 s3, s14, s16
	s_sub_i32 s2, s2, s3
	s_add_i32 s15, s2, s15
	s_ashr_i32 s16, s15, 4
	s_and_b64 s[2:3], s[4:5], exec
	s_cselect_b32 s2, s16, 0
	s_add_i32 s16, s2, s15
.LBB0_1110:
	v_mov_b32_e32 v0, 0
	s_mov_b32 s15, -2
	s_mov_b64 s[2:3], 0
	v_mov_b32_e32 v1, v0
	s_waitcnt lgkmcnt(0)
	s_add_u32 s66, s26, s2
	s_addc_u32 s67, s27, s3
	s_nop 0
	s_add_u32 s20, s66, 0x100
	s_addc_u32 s21, s67, 0
	s_add_u32 s18, s66, 0x180
	s_addc_u32 s19, s67, 0
	s_add_u32 s17, s24, s2
	s_addc_u32 s33, s25, s3
	s_add_u32 s34, s17, 0x100
	s_addc_u32 s35, s33, 0
	s_add_u32 s64, s66, 0x40080
	s_addc_u32 s65, s67, 0
	s_mov_b32 m0, s62
	s_nop 0
	global_load_lds_dwordx4 v65, s[64:65]
	s_nop 0
	s_mov_b32 m0, s63
	s_nop 0
	global_load_lds_dwordx4 v202, s[64:65]
	s_waitcnt vmcnt(8)
	s_waitcnt lgkmcnt(0)
	s_barrier
	s_setprio 1
	s_waitcnt lgkmcnt(0)
	v_mfma_f32_16x16x32_bf16 v[128:131], v[136:139], v[168:171], 0
	v_mfma_f32_16x16x32_bf16 v[124:127], v[144:147], v[168:171], 0
	v_mfma_f32_16x16x32_bf16 v[120:123], v[136:139], v[176:179], 0
	v_mfma_f32_16x16x32_bf16 v[116:119], v[144:147], v[176:179], 0
	v_mfma_f32_16x16x32_bf16 v[110:113], v[136:139], v[184:187], 0
	v_mfma_f32_16x16x32_bf16 v[106:109], v[144:147], v[184:187], 0
	v_mfma_f32_16x16x32_bf16 v[102:105], v[136:139], v[194:197], 0
	v_mfma_f32_16x16x32_bf16 v[98:101], v[144:147], v[194:197], 0
	v_mfma_f32_16x16x32_bf16 v[128:131], v[140:143], v[172:175], v[128:131]
	v_mfma_f32_16x16x32_bf16 v[124:127], v[148:151], v[172:175], v[124:127]
	v_mfma_f32_16x16x32_bf16 v[120:123], v[140:143], v[180:183], v[120:123]
	v_mfma_f32_16x16x32_bf16 v[116:119], v[148:151], v[180:183], v[116:119]
	v_mfma_f32_16x16x32_bf16 v[110:113], v[140:143], v[188:191], v[110:113]
	v_mfma_f32_16x16x32_bf16 v[106:109], v[148:151], v[188:191], v[106:109]
	v_mfma_f32_16x16x32_bf16 v[102:105], v[140:143], v[198:201], v[102:105]
	v_mfma_f32_16x16x32_bf16 v[98:101], v[148:151], v[198:201], v[98:101]
	s_setprio 0
	s_setprio 1
	v_mfma_f32_16x16x32_bf16 v[94:97], v[152:155], v[168:171], 0
	v_mfma_f32_16x16x32_bf16 v[90:93], v[160:163], v[168:171], 0
	v_mfma_f32_16x16x32_bf16 v[86:89], v[152:155], v[176:179], 0
	v_mfma_f32_16x16x32_bf16 v[82:85], v[160:163], v[176:179], 0
	v_mfma_f32_16x16x32_bf16 v[78:81], v[152:155], v[184:187], 0
	v_mfma_f32_16x16x32_bf16 v[74:77], v[160:163], v[184:187], 0
	v_mfma_f32_16x16x32_bf16 v[70:73], v[152:155], v[194:197], 0
	v_mfma_f32_16x16x32_bf16 v[66:69], v[160:163], v[194:197], 0
	v_mfma_f32_16x16x32_bf16 v[94:97], v[156:159], v[172:175], v[94:97]
	v_mfma_f32_16x16x32_bf16 v[90:93], v[164:167], v[172:175], v[90:93]
	v_mfma_f32_16x16x32_bf16 v[86:89], v[156:159], v[180:183], v[86:89]
	v_mfma_f32_16x16x32_bf16 v[82:85], v[164:167], v[180:183], v[82:85]
	v_mfma_f32_16x16x32_bf16 v[78:81], v[156:159], v[188:191], v[78:81]
	v_mfma_f32_16x16x32_bf16 v[74:77], v[164:167], v[188:191], v[74:77]
	v_mfma_f32_16x16x32_bf16 v[70:73], v[156:159], v[198:201], v[70:73]
	v_mfma_f32_16x16x32_bf16 v[66:69], v[164:167], v[198:201], v[66:69]
	s_setprio 0
	s_barrier
	ds_read_b128 v[168:171], v205 offset:16384
	ds_read_b128 v[172:175], v205 offset:17408
	ds_read_b128 v[176:179], v205 offset:18432
	ds_read_b128 v[180:183], v205 offset:19456
	ds_read_b128 v[184:187], v205 offset:20480
	ds_read_b128 v[188:191], v205 offset:21504
	ds_read_b128 v[194:197], v205 offset:22528
	ds_read_b128 v[198:201], v205 offset:23552
	s_mov_b32 m0, s44
	s_nop 0
	global_load_lds_dwordx4 v114, s[34:35]
	s_nop 0
	s_mov_b32 m0, s45
	s_nop 0
	global_load_lds_dwordx4 v203, s[34:35]
	s_add_u32 s34, s17, 0x40100
	s_addc_u32 s35, s33, 0
	s_mov_b32 m0, s46
	s_nop 0
	global_load_lds_dwordx4 v114, s[34:35]
	s_nop 0
	s_mov_b32 m0, s47
	s_nop 0
	global_load_lds_dwordx4 v203, s[34:35]
	s_mov_b32 m0, s43
	s_nop 0
	global_load_lds_dwordx4 v65, s[20:21]
	s_nop 0
	s_mov_b32 m0, s48
	s_nop 0
	global_load_lds_dwordx4 v202, s[20:21]
	s_waitcnt vmcnt(8)
	s_waitcnt lgkmcnt(0)
	s_barrier
	s_setprio 1
	s_waitcnt lgkmcnt(7)
	v_mfma_f32_16x16x32_bf16 v[60:63], v[136:139], v[168:171], 0
	v_mfma_f32_16x16x32_bf16 v[56:59], v[144:147], v[168:171], 0
	s_waitcnt lgkmcnt(5)
	v_mfma_f32_16x16x32_bf16 v[52:55], v[136:139], v[176:179], 0
	v_mfma_f32_16x16x32_bf16 v[48:51], v[144:147], v[176:179], 0
	s_waitcnt lgkmcnt(3)
	v_mfma_f32_16x16x32_bf16 v[44:47], v[136:139], v[184:187], 0
	v_mfma_f32_16x16x32_bf16 v[40:43], v[144:147], v[184:187], 0
	s_waitcnt lgkmcnt(1)
	v_mfma_f32_16x16x32_bf16 v[36:39], v[136:139], v[194:197], 0
	v_mfma_f32_16x16x32_bf16 v[32:35], v[144:147], v[194:197], 0
	v_mfma_f32_16x16x32_bf16 v[60:63], v[140:143], v[172:175], v[60:63]
	v_mfma_f32_16x16x32_bf16 v[56:59], v[148:151], v[172:175], v[56:59]
	v_mfma_f32_16x16x32_bf16 v[52:55], v[140:143], v[180:183], v[52:55]
	v_mfma_f32_16x16x32_bf16 v[48:51], v[148:151], v[180:183], v[48:51]
	v_mfma_f32_16x16x32_bf16 v[44:47], v[140:143], v[188:191], v[44:47]
	v_mfma_f32_16x16x32_bf16 v[40:43], v[148:151], v[188:191], v[40:43]
	s_waitcnt lgkmcnt(0)
	v_mfma_f32_16x16x32_bf16 v[36:39], v[140:143], v[198:201], v[36:39]
	v_mfma_f32_16x16x32_bf16 v[32:35], v[148:151], v[198:201], v[32:35]
	s_setprio 0
	s_setprio 1
	v_mfma_f32_16x16x32_bf16 v[28:31], v[152:155], v[168:171], 0
	v_mfma_f32_16x16x32_bf16 v[24:27], v[160:163], v[168:171], 0
	v_mfma_f32_16x16x32_bf16 v[20:23], v[152:155], v[176:179], 0
	v_mfma_f32_16x16x32_bf16 v[16:19], v[160:163], v[176:179], 0
	v_mfma_f32_16x16x32_bf16 v[12:15], v[152:155], v[184:187], 0
	v_mfma_f32_16x16x32_bf16 v[8:11], v[160:163], v[184:187], 0
	v_mfma_f32_16x16x32_bf16 v[4:7], v[152:155], v[194:197], 0
	v_mfma_f32_16x16x32_bf16 v[0:3], v[160:163], v[194:197], 0
	v_mfma_f32_16x16x32_bf16 v[28:31], v[156:159], v[172:175], v[28:31]
	v_mfma_f32_16x16x32_bf16 v[24:27], v[164:167], v[172:175], v[24:27]
	v_mfma_f32_16x16x32_bf16 v[20:23], v[156:159], v[180:183], v[20:23]
	v_mfma_f32_16x16x32_bf16 v[16:19], v[164:167], v[180:183], v[16:19]
	v_mfma_f32_16x16x32_bf16 v[12:15], v[156:159], v[188:191], v[12:15]
	v_mfma_f32_16x16x32_bf16 v[8:11], v[164:167], v[188:191], v[8:11]
	v_mfma_f32_16x16x32_bf16 v[4:7], v[156:159], v[198:201], v[4:7]
	v_mfma_f32_16x16x32_bf16 v[0:3], v[164:167], v[198:201], v[0:3]
	s_setprio 0
	s_barrier
	v_add_u32_e32 v133, 0x18000, v204
	v_add_u32_e32 v135, 0x1c000, v204
	ds_read_b128 v[136:139], v133
	ds_read_b128 v[140:143], v133 offset:1024
	ds_read_b128 v[144:147], v133 offset:2048
	ds_read_b128 v[148:151], v133 offset:3072
	ds_read_b128 v[152:155], v135
	ds_read_b128 v[156:159], v135 offset:1024
	ds_read_b128 v[160:163], v135 offset:2048
	ds_read_b128 v[164:167], v135 offset:3072
	ds_read_b128 v[168:171], v205 offset:32768
	ds_read_b128 v[172:175], v205 offset:33792
	ds_read_b128 v[176:179], v205 offset:34816
	ds_read_b128 v[180:183], v205 offset:35840
	ds_read_b128 v[184:187], v205 offset:36864
	ds_read_b128 v[188:191], v205 offset:37888
	ds_read_b128 v[194:197], v205 offset:38912
	ds_read_b128 v[198:201], v205 offset:39936
	s_add_u32 s20, s66, 0x40100
	s_addc_u32 s21, s67, 0
	s_mov_b32 m0, s49
	s_nop 0
	global_load_lds_dwordx4 v65, s[20:21]
	s_nop 0
	s_mov_b32 m0, s50
	s_nop 0
	global_load_lds_dwordx4 v202, s[20:21]
	s_waitcnt vmcnt(8)
	s_waitcnt lgkmcnt(0)
	s_barrier
	s_setprio 1
	s_waitcnt lgkmcnt(7)
	v_mfma_f32_16x16x32_bf16 v[128:131], v[136:139], v[168:171], v[128:131]
	v_mfma_f32_16x16x32_bf16 v[124:127], v[144:147], v[168:171], v[124:127]
	s_waitcnt lgkmcnt(5)
	v_mfma_f32_16x16x32_bf16 v[120:123], v[136:139], v[176:179], v[120:123]
	v_mfma_f32_16x16x32_bf16 v[116:119], v[144:147], v[176:179], v[116:119]
	s_waitcnt lgkmcnt(3)
	v_mfma_f32_16x16x32_bf16 v[110:113], v[136:139], v[184:187], v[110:113]
	v_mfma_f32_16x16x32_bf16 v[106:109], v[144:147], v[184:187], v[106:109]
	s_waitcnt lgkmcnt(1)
	v_mfma_f32_16x16x32_bf16 v[102:105], v[136:139], v[194:197], v[102:105]
	v_mfma_f32_16x16x32_bf16 v[98:101], v[144:147], v[194:197], v[98:101]
	v_mfma_f32_16x16x32_bf16 v[128:131], v[140:143], v[172:175], v[128:131]
	v_mfma_f32_16x16x32_bf16 v[124:127], v[148:151], v[172:175], v[124:127]
	v_mfma_f32_16x16x32_bf16 v[120:123], v[140:143], v[180:183], v[120:123]
	v_mfma_f32_16x16x32_bf16 v[116:119], v[148:151], v[180:183], v[116:119]
	v_mfma_f32_16x16x32_bf16 v[110:113], v[140:143], v[188:191], v[110:113]
	v_mfma_f32_16x16x32_bf16 v[106:109], v[148:151], v[188:191], v[106:109]
	s_waitcnt lgkmcnt(0)
	v_mfma_f32_16x16x32_bf16 v[102:105], v[140:143], v[198:201], v[102:105]
	v_mfma_f32_16x16x32_bf16 v[98:101], v[148:151], v[198:201], v[98:101]
	s_setprio 0
	s_setprio 1
	v_mfma_f32_16x16x32_bf16 v[94:97], v[152:155], v[168:171], v[94:97]
	v_mfma_f32_16x16x32_bf16 v[90:93], v[160:163], v[168:171], v[90:93]
	v_mfma_f32_16x16x32_bf16 v[86:89], v[152:155], v[176:179], v[86:89]
	v_mfma_f32_16x16x32_bf16 v[82:85], v[160:163], v[176:179], v[82:85]
	v_mfma_f32_16x16x32_bf16 v[78:81], v[152:155], v[184:187], v[78:81]
	v_mfma_f32_16x16x32_bf16 v[74:77], v[160:163], v[184:187], v[74:77]
	v_mfma_f32_16x16x32_bf16 v[70:73], v[152:155], v[194:197], v[70:73]
	v_mfma_f32_16x16x32_bf16 v[66:69], v[160:163], v[194:197], v[66:69]
	v_mfma_f32_16x16x32_bf16 v[94:97], v[156:159], v[172:175], v[94:97]
	v_mfma_f32_16x16x32_bf16 v[90:93], v[164:167], v[172:175], v[90:93]
	v_mfma_f32_16x16x32_bf16 v[86:89], v[156:159], v[180:183], v[86:89]
	v_mfma_f32_16x16x32_bf16 v[82:85], v[164:167], v[180:183], v[82:85]
	v_mfma_f32_16x16x32_bf16 v[78:81], v[156:159], v[188:191], v[78:81]
	v_mfma_f32_16x16x32_bf16 v[74:77], v[164:167], v[188:191], v[74:77]
	v_mfma_f32_16x16x32_bf16 v[70:73], v[156:159], v[198:201], v[70:73]
	v_mfma_f32_16x16x32_bf16 v[66:69], v[164:167], v[198:201], v[66:69]
	s_setprio 0
	s_barrier
	ds_read_b128 v[168:171], v205 offset:49152
	ds_read_b128 v[172:175], v205 offset:50176
	ds_read_b128 v[176:179], v205 offset:51200
	ds_read_b128 v[180:183], v205 offset:52224
	ds_read_b128 v[184:187], v205 offset:53248
	ds_read_b128 v[188:191], v205 offset:54272
	ds_read_b128 v[194:197], v205 offset:55296
	ds_read_b128 v[198:201], v205 offset:56320
	s_add_u32 s20, s17, 0x180
	s_addc_u32 s21, s33, 0
	s_mov_b32 m0, s56
	s_nop 0
	global_load_lds_dwordx4 v114, s[20:21]
	s_nop 0
	s_mov_b32 m0, s57
	s_nop 0
	global_load_lds_dwordx4 v203, s[20:21]
	s_add_u32 s20, s17, 0x40180
	s_addc_u32 s21, s33, 0
	s_mov_b32 m0, s60
	s_nop 0
	global_load_lds_dwordx4 v114, s[20:21]
	s_nop 0
	s_mov_b32 m0, s61
	s_nop 0
	global_load_lds_dwordx4 v203, s[20:21]
	s_nop 0
	s_mov_b32 m0, s58
	s_nop 0
	global_load_lds_dwordx4 v65, s[18:19]
	s_nop 0
	s_mov_b32 m0, s59
	s_nop 0
	global_load_lds_dwordx4 v202, s[18:19]
	s_waitcnt vmcnt(8)
	s_waitcnt lgkmcnt(0)
	s_barrier
	s_setprio 1
	s_waitcnt lgkmcnt(7)
	v_mfma_f32_16x16x32_bf16 v[60:63], v[136:139], v[168:171], v[60:63]
	v_mfma_f32_16x16x32_bf16 v[56:59], v[144:147], v[168:171], v[56:59]
	s_waitcnt lgkmcnt(5)
	v_mfma_f32_16x16x32_bf16 v[52:55], v[136:139], v[176:179], v[52:55]
	v_mfma_f32_16x16x32_bf16 v[48:51], v[144:147], v[176:179], v[48:51]
	s_waitcnt lgkmcnt(3)
	v_mfma_f32_16x16x32_bf16 v[44:47], v[136:139], v[184:187], v[44:47]
	v_mfma_f32_16x16x32_bf16 v[40:43], v[144:147], v[184:187], v[40:43]
	s_waitcnt lgkmcnt(1)
	v_mfma_f32_16x16x32_bf16 v[36:39], v[136:139], v[194:197], v[36:39]
	v_mfma_f32_16x16x32_bf16 v[32:35], v[144:147], v[194:197], v[32:35]
	v_mfma_f32_16x16x32_bf16 v[60:63], v[140:143], v[172:175], v[60:63]
	v_mfma_f32_16x16x32_bf16 v[56:59], v[148:151], v[172:175], v[56:59]
	v_mfma_f32_16x16x32_bf16 v[52:55], v[140:143], v[180:183], v[52:55]
	v_mfma_f32_16x16x32_bf16 v[48:51], v[148:151], v[180:183], v[48:51]
	v_mfma_f32_16x16x32_bf16 v[44:47], v[140:143], v[188:191], v[44:47]
	v_mfma_f32_16x16x32_bf16 v[40:43], v[148:151], v[188:191], v[40:43]
	s_waitcnt lgkmcnt(0)
	v_mfma_f32_16x16x32_bf16 v[36:39], v[140:143], v[198:201], v[36:39]
	v_mfma_f32_16x16x32_bf16 v[32:35], v[148:151], v[198:201], v[32:35]
	s_setprio 0
	s_setprio 1
	v_mfma_f32_16x16x32_bf16 v[28:31], v[152:155], v[168:171], v[28:31]
	v_mfma_f32_16x16x32_bf16 v[24:27], v[160:163], v[168:171], v[24:27]
	v_mfma_f32_16x16x32_bf16 v[20:23], v[152:155], v[176:179], v[20:23]
	v_mfma_f32_16x16x32_bf16 v[16:19], v[160:163], v[176:179], v[16:19]
	v_mfma_f32_16x16x32_bf16 v[12:15], v[152:155], v[184:187], v[12:15]
	v_mfma_f32_16x16x32_bf16 v[8:11], v[160:163], v[184:187], v[8:11]
	v_mfma_f32_16x16x32_bf16 v[4:7], v[152:155], v[194:197], v[4:7]
	v_mfma_f32_16x16x32_bf16 v[0:3], v[160:163], v[194:197], v[0:3]
	v_mfma_f32_16x16x32_bf16 v[28:31], v[156:159], v[172:175], v[28:31]
	v_mfma_f32_16x16x32_bf16 v[24:27], v[164:167], v[172:175], v[24:27]
	v_mfma_f32_16x16x32_bf16 v[20:23], v[156:159], v[180:183], v[20:23]
	v_mfma_f32_16x16x32_bf16 v[16:19], v[164:167], v[180:183], v[16:19]
	v_mfma_f32_16x16x32_bf16 v[12:15], v[156:159], v[188:191], v[12:15]
	v_mfma_f32_16x16x32_bf16 v[8:11], v[164:167], v[188:191], v[8:11]
	v_mfma_f32_16x16x32_bf16 v[4:7], v[156:159], v[198:201], v[4:7]
	v_mfma_f32_16x16x32_bf16 v[0:3], v[164:167], v[198:201], v[0:3]
	s_setprio 0
	s_barrier
	s_add_i32 s15, s15, 2
	s_add_u32 s2, s2, 0x100
	s_addc_u32 s3, s3, 0
	s_cmp_lt_u32 s15, 12

.LBB0_1418:
	v_add_u32_e32 v141, 0x10000, v134
	v_add_u32_e32 v142, 0x14000, v134
	ds_read_b128 v[144:147], v141
	ds_read_b128 v[148:151], v141 offset:1024
	ds_read_b128 v[152:155], v141 offset:2048
	ds_read_b128 v[156:159], v141 offset:3072
	ds_read_b128 v[160:163], v142
	ds_read_b128 v[164:167], v142 offset:1024
	ds_read_b128 v[168:171], v142 offset:2048
	ds_read_b128 v[172:175], v142 offset:3072
	ds_read_b128 v[176:179], v135
	ds_read_b128 v[180:183], v135 offset:1024
	ds_read_b128 v[184:187], v135 offset:2048
	ds_read_b128 v[188:191], v135 offset:3072
	ds_read_b128 v[194:197], v135 offset:4096
	ds_read_b128 v[198:201], v135 offset:5120
	ds_read_b128 v[202:205], v135 offset:6144
	ds_read_b128 v[206:209], v135 offset:7168
	s_add_i32 s59, s59, 1
	v_readlane_b32 s0, v254, 38
	s_mul_i32 s0, s59, s0
	s_mul_hi_u32 s1, s59, s70
	s_add_i32 s1, s1, s0
	s_mul_i32 s0, s59, s70
	v_readlane_b32 s2, v255, 0
	s_add_u32 s0, s0, s2
	s_addc_u32 s1, s1, s48
	v_mov_b64_e32 v[0:1], s[30:31]
	v_cmp_ge_i64_e32 vcc, s[0:1], v[0:1]
	v_cmp_lt_i64_e64 s[4:5], s[0:1], v[0:1]
	s_nop 3
	s_cmp_lg_u64 s[4:5], 0
	s_cselect_b64 s[100:101], -1, 1
	s_cbranch_vccnz .LBB0_1420
	s_ashr_i32 s1, s0, 31
	s_lshr_b32 s1, s1, 29
	s_add_i32 s1, s0, s1
	s_ashr_i32 s2, s1, 3
	s_and_b32 s1, s1, -8
	s_sub_i32 s0, s0, s1
	s_cmp_lt_i32 s0, 0
	s_cselect_b32 s1, s39, s29
	s_mul_i32 s0, s1, s0
	s_add_i32 s0, s0, s2
	s_ashr_i32 s1, s0, 31
	s_lshr_b32 s1, s1, 26
	s_add_i32 s1, s0, s1
	s_ashr_i32 s2, s1, 6
	s_lshl_b32 s2, s2, 3
	s_sub_i32 s3, s29, s2
	s_min_i32 s3, s3, 8
	s_abs_i32 s20, s3
	v_cvt_f32_u32_e32 v0, s20
	s_sub_i32 s22, 0, s20
	s_andn2_b32 s1, s1, 63
	s_sub_i32 s0, s0, s1
	v_rcp_iflag_f32_e32 v0, v0
	s_abs_i32 s1, s0
	s_xor_b32 s21, s0, s3
	s_ashr_i32 s21, s21, 31
	v_mul_f32_e32 v0, 0x4f7ffffe, v0
	v_cvt_u32_f32_e32 v0, v0
	s_nop 0
	v_readfirstlane_b32 s23, v0
	s_mul_i32 s22, s22, s23
	s_mul_hi_u32 s22, s23, s22
	s_add_i32 s23, s23, s22
	s_mul_hi_u32 s22, s1, s23
	s_mul_i32 s23, s22, s20
	s_sub_i32 s1, s1, s23
	s_add_i32 s26, s22, 1
	s_sub_i32 s23, s1, s20
	s_cmp_ge_u32 s1, s20
	s_cselect_b32 s22, s26, s22
	s_cselect_b32 s1, s23, s1
	s_add_i32 s23, s22, 1
	s_cmp_ge_u32 s1, s20
	s_cselect_b32 s1, s23, s22
	s_xor_b32 s1, s1, s21
	s_sub_i32 s20, s1, s21
	s_mul_i32 s1, s20, s3
	s_sub_i32 s0, s0, s1
	s_add_i32 s60, s0, s2

.LBB0_1424:
	v_mov_b32_e32 v0, 0
	v_readlane_b32 s72, v254, 62
	s_mov_b32 s21, -2
	s_mov_b64 s[2:3], 0
	v_mov_b32_e32 v1, v0
	v_readlane_b32 s73, v254, 63
	s_add_u32 s66, s72, s2
	s_addc_u32 s67, s73, s3
	s_add_u32 s34, s66, 0x2000100
	s_addc_u32 s35, s67, 0
	s_add_u32 s26, s66, 0x2000180
	s_addc_u32 s27, s67, 0
	s_add_u32 s33, s24, s2
	s_addc_u32 s63, s25, s3
	s_add_u32 s64, s33, 0x100
	s_addc_u32 s65, s63, 0
	s_add_u32 s66, s66, 0x2000080
	s_addc_u32 s67, s67, 0
	s_mov_b32 m0, s57
	s_nop 0
	global_load_lds_dwordx4 v133, s[66:67]
	s_nop 0
	s_mov_b32 m0, s58
	s_nop 0
	global_load_lds_dwordx4 v132, s[66:67]
	s_waitcnt vmcnt(8)
	s_waitcnt lgkmcnt(0)
	s_barrier
	s_setprio 1
	s_waitcnt lgkmcnt(0)
	v_mfma_f32_16x16x32_bf16 v[128:131], v[144:147], v[176:179], 0
	v_mfma_f32_16x16x32_bf16 v[124:127], v[152:155], v[176:179], 0
	s_waitcnt lgkmcnt(5)
	v_mfma_f32_16x16x32_bf16 v[120:123], v[144:147], v[184:187], 0
	v_mfma_f32_16x16x32_bf16 v[116:119], v[152:155], v[184:187], 0
	s_waitcnt lgkmcnt(3)
	v_mfma_f32_16x16x32_bf16 v[110:113], v[144:147], v[194:197], 0
	v_mfma_f32_16x16x32_bf16 v[106:109], v[152:155], v[194:197], 0
	s_waitcnt lgkmcnt(1)
	v_mfma_f32_16x16x32_bf16 v[102:105], v[144:147], v[202:205], 0
	v_mfma_f32_16x16x32_bf16 v[98:101], v[152:155], v[202:205], 0
	v_mfma_f32_16x16x32_bf16 v[128:131], v[148:151], v[180:183], v[128:131]
	v_mfma_f32_16x16x32_bf16 v[124:127], v[156:159], v[180:183], v[124:127]
	v_mfma_f32_16x16x32_bf16 v[120:123], v[148:151], v[188:191], v[120:123]
	v_mfma_f32_16x16x32_bf16 v[116:119], v[156:159], v[188:191], v[116:119]
	v_mfma_f32_16x16x32_bf16 v[110:113], v[148:151], v[198:201], v[110:113]
	v_mfma_f32_16x16x32_bf16 v[106:109], v[156:159], v[198:201], v[106:109]
	s_waitcnt lgkmcnt(0)
	v_mfma_f32_16x16x32_bf16 v[102:105], v[148:151], v[206:209], v[102:105]
	v_mfma_f32_16x16x32_bf16 v[98:101], v[156:159], v[206:209], v[98:101]
	s_setprio 0
	s_setprio 1
	v_mfma_f32_16x16x32_bf16 v[94:97], v[160:163], v[176:179], 0
	v_mfma_f32_16x16x32_bf16 v[90:93], v[168:171], v[176:179], 0
	v_mfma_f32_16x16x32_bf16 v[86:89], v[160:163], v[184:187], 0
	v_mfma_f32_16x16x32_bf16 v[82:85], v[168:171], v[184:187], 0
	v_mfma_f32_16x16x32_bf16 v[78:81], v[160:163], v[194:197], 0
	v_mfma_f32_16x16x32_bf16 v[74:77], v[168:171], v[194:197], 0
	v_mfma_f32_16x16x32_bf16 v[70:73], v[160:163], v[202:205], 0
	v_mfma_f32_16x16x32_bf16 v[66:69], v[168:171], v[202:205], 0
	v_mfma_f32_16x16x32_bf16 v[94:97], v[164:167], v[180:183], v[94:97]
	v_mfma_f32_16x16x32_bf16 v[90:93], v[172:175], v[180:183], v[90:93]
	v_mfma_f32_16x16x32_bf16 v[86:89], v[164:167], v[188:191], v[86:89]
	v_mfma_f32_16x16x32_bf16 v[82:85], v[172:175], v[188:191], v[82:85]
	v_mfma_f32_16x16x32_bf16 v[78:81], v[164:167], v[198:201], v[78:81]
	v_mfma_f32_16x16x32_bf16 v[74:77], v[172:175], v[198:201], v[74:77]
	v_mfma_f32_16x16x32_bf16 v[70:73], v[164:167], v[206:209], v[70:73]
	v_mfma_f32_16x16x32_bf16 v[66:69], v[172:175], v[206:209], v[66:69]
	s_setprio 0
	s_barrier
	ds_read_b128 v[176:179], v135 offset:16384
	ds_read_b128 v[180:183], v135 offset:17408
	ds_read_b128 v[184:187], v135 offset:18432
	ds_read_b128 v[188:191], v135 offset:19456
	ds_read_b128 v[194:197], v135 offset:20480
	ds_read_b128 v[198:201], v135 offset:21504
	ds_read_b128 v[202:205], v135 offset:22528
	ds_read_b128 v[206:209], v135 offset:23552
	s_mov_b32 m0, s41
	s_nop 0
	global_load_lds_dwordx4 v65, s[64:65]
	s_nop 0
	s_mov_b32 m0, s42
	s_nop 0
	global_load_lds_dwordx4 v114, s[64:65]
	s_add_u32 s64, s33, 0x40100
	s_addc_u32 s65, s63, 0
	s_mov_b32 m0, s43
	s_nop 0
	global_load_lds_dwordx4 v65, s[64:65]
	s_nop 0
	s_mov_b32 m0, s44
	s_nop 0
	global_load_lds_dwordx4 v114, s[64:65]
	s_mov_b32 m0, s40
	s_nop 0
	global_load_lds_dwordx4 v139, s[34:35]
	s_nop 0
	s_mov_b32 m0, s45
	s_nop 0
	global_load_lds_dwordx4 v138, s[34:35]
	s_waitcnt vmcnt(8)
	s_waitcnt lgkmcnt(0)
	s_barrier
	s_setprio 1
	s_waitcnt lgkmcnt(0)
	v_mfma_f32_16x16x32_bf16 v[60:63], v[144:147], v[176:179], 0
	v_mfma_f32_16x16x32_bf16 v[56:59], v[152:155], v[176:179], 0
	s_waitcnt lgkmcnt(5)
	v_mfma_f32_16x16x32_bf16 v[52:55], v[144:147], v[184:187], 0
	v_mfma_f32_16x16x32_bf16 v[48:51], v[152:155], v[184:187], 0
	s_waitcnt lgkmcnt(3)
	v_mfma_f32_16x16x32_bf16 v[44:47], v[144:147], v[194:197], 0
	v_mfma_f32_16x16x32_bf16 v[40:43], v[152:155], v[194:197], 0
	s_waitcnt lgkmcnt(1)
	v_mfma_f32_16x16x32_bf16 v[36:39], v[144:147], v[202:205], 0
	v_mfma_f32_16x16x32_bf16 v[32:35], v[152:155], v[202:205], 0
	v_mfma_f32_16x16x32_bf16 v[60:63], v[148:151], v[180:183], v[60:63]
	v_mfma_f32_16x16x32_bf16 v[56:59], v[156:159], v[180:183], v[56:59]
	v_mfma_f32_16x16x32_bf16 v[52:55], v[148:151], v[188:191], v[52:55]
	v_mfma_f32_16x16x32_bf16 v[48:51], v[156:159], v[188:191], v[48:51]
	v_mfma_f32_16x16x32_bf16 v[44:47], v[148:151], v[198:201], v[44:47]
	v_mfma_f32_16x16x32_bf16 v[40:43], v[156:159], v[198:201], v[40:43]
	s_waitcnt lgkmcnt(0)
	v_mfma_f32_16x16x32_bf16 v[36:39], v[148:151], v[206:209], v[36:39]
	v_mfma_f32_16x16x32_bf16 v[32:35], v[156:159], v[206:209], v[32:35]
	s_setprio 0
	s_setprio 1
	v_mfma_f32_16x16x32_bf16 v[28:31], v[160:163], v[176:179], 0
	v_mfma_f32_16x16x32_bf16 v[24:27], v[168:171], v[176:179], 0
	v_mfma_f32_16x16x32_bf16 v[20:23], v[160:163], v[184:187], 0
	v_mfma_f32_16x16x32_bf16 v[16:19], v[168:171], v[184:187], 0
	v_mfma_f32_16x16x32_bf16 v[12:15], v[160:163], v[194:197], 0
	v_mfma_f32_16x16x32_bf16 v[8:11], v[168:171], v[194:197], 0
	v_mfma_f32_16x16x32_bf16 v[4:7], v[160:163], v[202:205], 0
	v_mfma_f32_16x16x32_bf16 v[0:3], v[168:171], v[202:205], 0
	v_mfma_f32_16x16x32_bf16 v[28:31], v[164:167], v[180:183], v[28:31]
	v_mfma_f32_16x16x32_bf16 v[24:27], v[172:175], v[180:183], v[24:27]
	v_mfma_f32_16x16x32_bf16 v[20:23], v[164:167], v[188:191], v[20:23]
	v_mfma_f32_16x16x32_bf16 v[16:19], v[172:175], v[188:191], v[16:19]
	v_mfma_f32_16x16x32_bf16 v[12:15], v[164:167], v[198:201], v[12:15]
	v_mfma_f32_16x16x32_bf16 v[8:11], v[172:175], v[198:201], v[8:11]
	v_mfma_f32_16x16x32_bf16 v[4:7], v[164:167], v[206:209], v[4:7]
	v_mfma_f32_16x16x32_bf16 v[0:3], v[172:175], v[206:209], v[0:3]
	s_setprio 0
	s_barrier
	v_add_u32_e32 v143, 0x18000, v134
	v_add_u32_e32 v144, 0x1c000, v134
	ds_read_b128 v[146:149], v143
	ds_read_b128 v[150:153], v143 offset:1024
	ds_read_b128 v[154:157], v143 offset:2048
	ds_read_b128 v[158:161], v143 offset:3072
	ds_read_b128 v[162:165], v144
	ds_read_b128 v[166:169], v144 offset:1024
	ds_read_b128 v[170:173], v144 offset:2048
	ds_read_b128 v[174:177], v144 offset:3072
	ds_read_b128 v[178:181], v135 offset:32768
	ds_read_b128 v[182:185], v135 offset:33792
	ds_read_b128 v[186:189], v135 offset:34816
	ds_read_b128 v[194:197], v135 offset:35840
	ds_read_b128 v[198:201], v135 offset:36864
	ds_read_b128 v[202:205], v135 offset:37888
	ds_read_b128 v[206:209], v135 offset:38912
	ds_read_b128 v[210:213], v135 offset:39936
	s_mov_b32 m0, s46
	s_nop 0
	global_load_lds_dwordx4 v133, s[34:35]
	s_nop 0
	s_mov_b32 m0, s47
	s_nop 0
	global_load_lds_dwordx4 v132, s[34:35]
	s_waitcnt vmcnt(8)
	s_waitcnt lgkmcnt(0)
	s_barrier
	s_setprio 1
	s_waitcnt lgkmcnt(0)
	v_mfma_f32_16x16x32_bf16 v[128:131], v[146:149], v[178:181], v[128:131]
	v_mfma_f32_16x16x32_bf16 v[124:127], v[154:157], v[178:181], v[124:127]
	s_waitcnt lgkmcnt(5)
	v_mfma_f32_16x16x32_bf16 v[120:123], v[146:149], v[186:189], v[120:123]
	v_mfma_f32_16x16x32_bf16 v[116:119], v[154:157], v[186:189], v[116:119]
	s_waitcnt lgkmcnt(3)
	v_mfma_f32_16x16x32_bf16 v[110:113], v[146:149], v[198:201], v[110:113]
	v_mfma_f32_16x16x32_bf16 v[106:109], v[154:157], v[198:201], v[106:109]
	s_waitcnt lgkmcnt(1)
	v_mfma_f32_16x16x32_bf16 v[102:105], v[146:149], v[206:209], v[102:105]
	v_mfma_f32_16x16x32_bf16 v[98:101], v[154:157], v[206:209], v[98:101]
	v_mfma_f32_16x16x32_bf16 v[128:131], v[150:153], v[182:185], v[128:131]
	v_mfma_f32_16x16x32_bf16 v[124:127], v[158:161], v[182:185], v[124:127]
	v_mfma_f32_16x16x32_bf16 v[120:123], v[150:153], v[194:197], v[120:123]
	v_mfma_f32_16x16x32_bf16 v[116:119], v[158:161], v[194:197], v[116:119]
	v_mfma_f32_16x16x32_bf16 v[110:113], v[150:153], v[202:205], v[110:113]
	v_mfma_f32_16x16x32_bf16 v[106:109], v[158:161], v[202:205], v[106:109]
	s_waitcnt lgkmcnt(0)
	v_mfma_f32_16x16x32_bf16 v[102:105], v[150:153], v[210:213], v[102:105]
	v_mfma_f32_16x16x32_bf16 v[98:101], v[158:161], v[210:213], v[98:101]
	s_setprio 0
	s_setprio 1
	v_mfma_f32_16x16x32_bf16 v[94:97], v[162:165], v[178:181], v[94:97]
	v_mfma_f32_16x16x32_bf16 v[90:93], v[170:173], v[178:181], v[90:93]
	v_mfma_f32_16x16x32_bf16 v[86:89], v[162:165], v[186:189], v[86:89]
	v_mfma_f32_16x16x32_bf16 v[82:85], v[170:173], v[186:189], v[82:85]
	v_mfma_f32_16x16x32_bf16 v[78:81], v[162:165], v[198:201], v[78:81]
	v_mfma_f32_16x16x32_bf16 v[74:77], v[170:173], v[198:201], v[74:77]
	v_mfma_f32_16x16x32_bf16 v[70:73], v[162:165], v[206:209], v[70:73]
	v_mfma_f32_16x16x32_bf16 v[66:69], v[170:173], v[206:209], v[66:69]
	v_mfma_f32_16x16x32_bf16 v[94:97], v[166:169], v[182:185], v[94:97]
	v_mfma_f32_16x16x32_bf16 v[90:93], v[174:177], v[182:185], v[90:93]
	v_mfma_f32_16x16x32_bf16 v[86:89], v[166:169], v[194:197], v[86:89]
	v_mfma_f32_16x16x32_bf16 v[82:85], v[174:177], v[194:197], v[82:85]
	v_mfma_f32_16x16x32_bf16 v[78:81], v[166:169], v[202:205], v[78:81]
	v_mfma_f32_16x16x32_bf16 v[74:77], v[174:177], v[202:205], v[74:77]
	v_mfma_f32_16x16x32_bf16 v[70:73], v[166:169], v[210:213], v[70:73]
	v_mfma_f32_16x16x32_bf16 v[66:69], v[174:177], v[210:213], v[66:69]
	s_setprio 0
	s_barrier
	ds_read_b128 v[178:181], v135 offset:49152
	ds_read_b128 v[182:185], v135 offset:50176
	ds_read_b128 v[186:189], v135 offset:51200
	ds_read_b128 v[194:197], v135 offset:52224
	ds_read_b128 v[198:201], v135 offset:53248
	ds_read_b128 v[202:205], v135 offset:54272
	ds_read_b128 v[206:209], v135 offset:55296
	ds_read_b128 v[210:213], v135 offset:56320
	s_add_u32 s34, s33, 0x180
	s_addc_u32 s35, s63, 0
	s_mov_b32 m0, s51
	s_nop 0
	global_load_lds_dwordx4 v65, s[34:35]
	s_nop 0
	s_mov_b32 m0, s52
	s_nop 0
	global_load_lds_dwordx4 v114, s[34:35]
	s_add_u32 s34, s33, 0x40180
	s_addc_u32 s35, s63, 0
	s_mov_b32 m0, s55
	s_nop 0
	global_load_lds_dwordx4 v65, s[34:35]
	s_nop 0
	s_mov_b32 m0, s56
	s_nop 0
	global_load_lds_dwordx4 v114, s[34:35]
	s_nop 0
	s_mov_b32 m0, s53
	s_nop 0
	global_load_lds_dwordx4 v139, s[26:27]
	s_nop 0
	s_mov_b32 m0, s54
	s_nop 0
	global_load_lds_dwordx4 v138, s[26:27]
	s_waitcnt vmcnt(8)
	s_waitcnt lgkmcnt(0)
	s_barrier
	s_setprio 1
	s_waitcnt lgkmcnt(0)
	v_mfma_f32_16x16x32_bf16 v[60:63], v[146:149], v[178:181], v[60:63]
	v_mfma_f32_16x16x32_bf16 v[56:59], v[154:157], v[178:181], v[56:59]
	s_waitcnt lgkmcnt(5)
	v_mfma_f32_16x16x32_bf16 v[52:55], v[146:149], v[186:189], v[52:55]
	v_mfma_f32_16x16x32_bf16 v[48:51], v[154:157], v[186:189], v[48:51]
	s_waitcnt lgkmcnt(3)
	v_mfma_f32_16x16x32_bf16 v[44:47], v[146:149], v[198:201], v[44:47]
	v_mfma_f32_16x16x32_bf16 v[40:43], v[154:157], v[198:201], v[40:43]
	s_waitcnt lgkmcnt(1)
	v_mfma_f32_16x16x32_bf16 v[36:39], v[146:149], v[206:209], v[36:39]
	v_mfma_f32_16x16x32_bf16 v[32:35], v[154:157], v[206:209], v[32:35]
	v_mfma_f32_16x16x32_bf16 v[60:63], v[150:153], v[182:185], v[60:63]
	v_mfma_f32_16x16x32_bf16 v[56:59], v[158:161], v[182:185], v[56:59]
	v_mfma_f32_16x16x32_bf16 v[52:55], v[150:153], v[194:197], v[52:55]
	v_mfma_f32_16x16x32_bf16 v[48:51], v[158:161], v[194:197], v[48:51]
	v_mfma_f32_16x16x32_bf16 v[44:47], v[150:153], v[202:205], v[44:47]
	v_mfma_f32_16x16x32_bf16 v[40:43], v[158:161], v[202:205], v[40:43]
	s_waitcnt lgkmcnt(0)
	v_mfma_f32_16x16x32_bf16 v[36:39], v[150:153], v[210:213], v[36:39]
	v_mfma_f32_16x16x32_bf16 v[32:35], v[158:161], v[210:213], v[32:35]
	s_setprio 0
	s_setprio 1
	v_mfma_f32_16x16x32_bf16 v[28:31], v[162:165], v[178:181], v[28:31]
	v_mfma_f32_16x16x32_bf16 v[24:27], v[170:173], v[178:181], v[24:27]
	v_mfma_f32_16x16x32_bf16 v[20:23], v[162:165], v[186:189], v[20:23]
	v_mfma_f32_16x16x32_bf16 v[16:19], v[170:173], v[186:189], v[16:19]
	v_mfma_f32_16x16x32_bf16 v[12:15], v[162:165], v[198:201], v[12:15]
	v_mfma_f32_16x16x32_bf16 v[8:11], v[170:173], v[198:201], v[8:11]
	v_mfma_f32_16x16x32_bf16 v[4:7], v[162:165], v[206:209], v[4:7]
	v_mfma_f32_16x16x32_bf16 v[0:3], v[170:173], v[206:209], v[0:3]
	v_mfma_f32_16x16x32_bf16 v[28:31], v[166:169], v[182:185], v[28:31]
	v_mfma_f32_16x16x32_bf16 v[24:27], v[174:177], v[182:185], v[24:27]
	v_mfma_f32_16x16x32_bf16 v[20:23], v[166:169], v[194:197], v[20:23]
	v_mfma_f32_16x16x32_bf16 v[16:19], v[174:177], v[194:197], v[16:19]
	v_mfma_f32_16x16x32_bf16 v[12:15], v[166:169], v[202:205], v[12:15]
	v_mfma_f32_16x16x32_bf16 v[8:11], v[174:177], v[202:205], v[8:11]
	v_mfma_f32_16x16x32_bf16 v[4:7], v[166:169], v[210:213], v[4:7]
	v_mfma_f32_16x16x32_bf16 v[0:3], v[174:177], v[210:213], v[0:3]
	s_setprio 0
	s_barrier
	s_add_i32 s21, s21, 2
	s_add_u32 s2, s2, 0x100
	s_addc_u32 s3, s3, 0
	s_cmp_lt_u32 s21, 12

.LBB0_1501:
	v_add_u32_e32 v132, 0x10000, v142
	v_add_u32_e32 v133, 0x14000, v142
	ds_read_b128 v[134:137], v132
	ds_read_b128 v[144:147], v132 offset:1024
	ds_read_b128 v[148:151], v132 offset:2048
	ds_read_b128 v[152:155], v132 offset:3072
	ds_read_b128 v[156:159], v133
	ds_read_b128 v[160:163], v133 offset:1024
	ds_read_b128 v[164:167], v133 offset:2048
	ds_read_b128 v[168:171], v133 offset:3072
	ds_read_b128 v[172:175], v143
	ds_read_b128 v[176:179], v143 offset:1024
	ds_read_b128 v[180:183], v143 offset:2048
	ds_read_b128 v[184:187], v143 offset:3072
	ds_read_b128 v[188:191], v143 offset:4096
	ds_read_b128 v[194:197], v143 offset:5120
	ds_read_b128 v[198:201], v143 offset:6144
	ds_read_b128 v[202:205], v143 offset:7168
	s_add_i32 s59, s59, 1
	v_readlane_b32 s0, v254, 38
	s_mul_i32 s0, s59, s0
	s_mul_hi_u32 s1, s59, s70
	s_add_i32 s1, s1, s0
	s_mul_i32 s0, s59, s70
	v_readlane_b32 s4, v255, 0
	s_add_u32 s0, s0, s4
	s_addc_u32 s1, s1, s49
	v_mov_b64_e32 v[0:1], s[30:31]
	v_cmp_ge_i64_e32 vcc, s[0:1], v[0:1]
	v_cmp_lt_i64_e64 s[4:5], s[0:1], v[0:1]
	s_nop 3
	s_cmp_lg_u64 s[4:5], 0
	s_cselect_b64 s[100:101], -1, 1
	s_cbranch_vccnz .LBB0_1503
	s_ashr_i32 s1, s0, 31
	s_lshr_b32 s1, s1, 29
	s_add_i32 s1, s0, s1
	s_ashr_i32 s12, s1, 3
	s_and_b32 s1, s1, -8
	s_sub_i32 s0, s0, s1
	s_lshr_b32 s1, s0, 31
	s_or_b32 s1, s48, s1
	s_mul_i32 s0, s1, s0
	s_add_i32 s0, s0, s12
	s_ashr_i32 s1, s0, 31
	s_lshr_b32 s1, s1, 27
	s_add_i32 s1, s0, s1
	s_ashr_i32 s12, s1, 5
	s_lshl_b32 s13, s12, 3
	s_sub_i32 s12, s29, s13
	s_min_i32 s14, s12, 8
	s_abs_i32 s12, s14
	v_cvt_f32_u32_e32 v0, s12
	s_sub_i32 s16, 0, s12
	s_andn2_b32 s1, s1, 31
	s_sub_i32 s0, s0, s1
	v_rcp_iflag_f32_e32 v0, v0
	s_abs_i32 s1, s0
	s_xor_b32 s15, s0, s14
	s_ashr_i32 s15, s15, 31
	v_mul_f32_e32 v0, 0x4f7ffffe, v0
	v_cvt_u32_f32_e32 v0, v0
	s_nop 0
	v_readfirstlane_b32 s17, v0
	s_mul_i32 s16, s16, s17
	s_mul_hi_u32 s16, s17, s16
	s_add_i32 s17, s17, s16
	s_mul_hi_u32 s16, s1, s17
	s_mul_i32 s17, s16, s12
	s_sub_i32 s1, s1, s17
	s_add_i32 s18, s16, 1
	s_sub_i32 s17, s1, s12
	s_cmp_ge_u32 s1, s12
	s_cselect_b32 s16, s18, s16
	s_cselect_b32 s1, s17, s1
	s_add_i32 s17, s16, 1
	s_cmp_ge_u32 s1, s12
	s_cselect_b32 s1, s17, s16
	s_xor_b32 s1, s1, s15
	s_sub_i32 s12, s1, s15
	s_mul_i32 s1, s12, s14
	s_sub_i32 s0, s0, s1
	s_add_i32 s14, s0, s13

.LBB0_1505:
	v_mov_b32_e32 v0, 0
	s_mov_b32 s13, -2
	s_mov_b64 s[18:19], 0
	v_mov_b32_e32 v1, v0
	s_waitcnt lgkmcnt(0)
	s_add_u32 s61, s22, s18
	s_addc_u32 s66, s23, s19
	s_add_u32 s34, s61, 0x100
	s_addc_u32 s35, s66, 0
	s_add_u32 s26, s61, 0x180
	s_addc_u32 s27, s66, 0
	s_add_u32 s15, s24, s18
	s_addc_u32 s33, s25, s19
	s_add_u32 s62, s15, 0x100
	s_addc_u32 s63, s33, 0
	s_add_u32 s64, s61, 0x40080
	s_addc_u32 s65, s66, 0
	s_mov_b32 m0, s57
	s_nop 0
	global_load_lds_dwordx4 v65, s[64:65]
	s_nop 0
	s_mov_b32 m0, s58
	s_nop 0
	global_load_lds_dwordx4 v140, s[64:65]
	s_waitcnt vmcnt(8)
	s_waitcnt lgkmcnt(0)
	s_barrier
	s_setprio 1
	s_waitcnt lgkmcnt(0)
	v_mfma_f32_16x16x32_bf16 v[128:131], v[134:137], v[172:175], 0
	v_mfma_f32_16x16x32_bf16 v[124:127], v[148:151], v[172:175], 0
	s_waitcnt lgkmcnt(5)
	v_mfma_f32_16x16x32_bf16 v[120:123], v[134:137], v[180:183], 0
	v_mfma_f32_16x16x32_bf16 v[116:119], v[148:151], v[180:183], 0
	s_waitcnt lgkmcnt(3)
	v_mfma_f32_16x16x32_bf16 v[110:113], v[134:137], v[188:191], 0
	v_mfma_f32_16x16x32_bf16 v[106:109], v[148:151], v[188:191], 0
	s_waitcnt lgkmcnt(1)
	v_mfma_f32_16x16x32_bf16 v[102:105], v[134:137], v[198:201], 0
	v_mfma_f32_16x16x32_bf16 v[98:101], v[148:151], v[198:201], 0
	v_mfma_f32_16x16x32_bf16 v[128:131], v[144:147], v[176:179], v[128:131]
	v_mfma_f32_16x16x32_bf16 v[124:127], v[152:155], v[176:179], v[124:127]
	v_mfma_f32_16x16x32_bf16 v[120:123], v[144:147], v[184:187], v[120:123]
	v_mfma_f32_16x16x32_bf16 v[116:119], v[152:155], v[184:187], v[116:119]
	v_mfma_f32_16x16x32_bf16 v[110:113], v[144:147], v[194:197], v[110:113]
	v_mfma_f32_16x16x32_bf16 v[106:109], v[152:155], v[194:197], v[106:109]
	s_waitcnt lgkmcnt(0)
	v_mfma_f32_16x16x32_bf16 v[102:105], v[144:147], v[202:205], v[102:105]
	v_mfma_f32_16x16x32_bf16 v[98:101], v[152:155], v[202:205], v[98:101]
	s_setprio 0
	s_setprio 1
	v_mfma_f32_16x16x32_bf16 v[94:97], v[156:159], v[172:175], 0
	v_mfma_f32_16x16x32_bf16 v[90:93], v[164:167], v[172:175], 0
	v_mfma_f32_16x16x32_bf16 v[86:89], v[156:159], v[180:183], 0
	v_mfma_f32_16x16x32_bf16 v[82:85], v[164:167], v[180:183], 0
	v_mfma_f32_16x16x32_bf16 v[78:81], v[156:159], v[188:191], 0
	v_mfma_f32_16x16x32_bf16 v[74:77], v[164:167], v[188:191], 0
	v_mfma_f32_16x16x32_bf16 v[70:73], v[156:159], v[198:201], 0
	v_mfma_f32_16x16x32_bf16 v[66:69], v[164:167], v[198:201], 0
	v_mfma_f32_16x16x32_bf16 v[94:97], v[160:163], v[176:179], v[94:97]
	v_mfma_f32_16x16x32_bf16 v[90:93], v[168:171], v[176:179], v[90:93]
	v_mfma_f32_16x16x32_bf16 v[86:89], v[160:163], v[184:187], v[86:89]
	v_mfma_f32_16x16x32_bf16 v[82:85], v[168:171], v[184:187], v[82:85]
	v_mfma_f32_16x16x32_bf16 v[78:81], v[160:163], v[194:197], v[78:81]
	v_mfma_f32_16x16x32_bf16 v[74:77], v[168:171], v[194:197], v[74:77]
	v_mfma_f32_16x16x32_bf16 v[70:73], v[160:163], v[202:205], v[70:73]
	v_mfma_f32_16x16x32_bf16 v[66:69], v[168:171], v[202:205], v[66:69]
	s_setprio 0
	s_barrier
	ds_read_b128 v[172:175], v143 offset:16384
	ds_read_b128 v[176:179], v143 offset:17408
	ds_read_b128 v[180:183], v143 offset:18432
	ds_read_b128 v[184:187], v143 offset:19456
	ds_read_b128 v[188:191], v143 offset:20480
	ds_read_b128 v[194:197], v143 offset:21504
	ds_read_b128 v[198:201], v143 offset:22528
	ds_read_b128 v[202:205], v143 offset:23552
	s_mov_b32 m0, s41
	s_nop 0
	global_load_lds_dwordx4 v114, s[62:63]
	s_nop 0
	s_mov_b32 m0, s42
	s_nop 0
	global_load_lds_dwordx4 v141, s[62:63]
	s_add_u32 s62, s15, 0x40100
	s_addc_u32 s63, s33, 0
	s_mov_b32 m0, s43
	s_nop 0
	global_load_lds_dwordx4 v114, s[62:63]
	s_nop 0
	s_mov_b32 m0, s44
	s_nop 0
	global_load_lds_dwordx4 v141, s[62:63]
	s_mov_b32 m0, s40
	s_nop 0
	global_load_lds_dwordx4 v65, s[34:35]
	s_nop 0
	s_mov_b32 m0, s45
	s_nop 0
	global_load_lds_dwordx4 v140, s[34:35]
	s_waitcnt vmcnt(8)
	s_waitcnt lgkmcnt(0)
	s_barrier
	s_setprio 1
	s_waitcnt lgkmcnt(0)
	v_mfma_f32_16x16x32_bf16 v[60:63], v[134:137], v[172:175], 0
	v_mfma_f32_16x16x32_bf16 v[56:59], v[148:151], v[172:175], 0
	s_waitcnt lgkmcnt(5)
	v_mfma_f32_16x16x32_bf16 v[52:55], v[134:137], v[180:183], 0
	v_mfma_f32_16x16x32_bf16 v[48:51], v[148:151], v[180:183], 0
	s_waitcnt lgkmcnt(3)
	v_mfma_f32_16x16x32_bf16 v[44:47], v[134:137], v[188:191], 0
	v_mfma_f32_16x16x32_bf16 v[40:43], v[148:151], v[188:191], 0
	s_waitcnt lgkmcnt(1)
	v_mfma_f32_16x16x32_bf16 v[36:39], v[134:137], v[198:201], 0
	v_mfma_f32_16x16x32_bf16 v[32:35], v[148:151], v[198:201], 0
	v_mfma_f32_16x16x32_bf16 v[60:63], v[144:147], v[176:179], v[60:63]
	v_mfma_f32_16x16x32_bf16 v[56:59], v[152:155], v[176:179], v[56:59]
	v_mfma_f32_16x16x32_bf16 v[52:55], v[144:147], v[184:187], v[52:55]
	v_mfma_f32_16x16x32_bf16 v[48:51], v[152:155], v[184:187], v[48:51]
	v_mfma_f32_16x16x32_bf16 v[44:47], v[144:147], v[194:197], v[44:47]
	v_mfma_f32_16x16x32_bf16 v[40:43], v[152:155], v[194:197], v[40:43]
	s_waitcnt lgkmcnt(0)
	v_mfma_f32_16x16x32_bf16 v[36:39], v[144:147], v[202:205], v[36:39]
	v_mfma_f32_16x16x32_bf16 v[32:35], v[152:155], v[202:205], v[32:35]
	s_setprio 0
	s_setprio 1
	v_mfma_f32_16x16x32_bf16 v[28:31], v[156:159], v[172:175], 0
	v_mfma_f32_16x16x32_bf16 v[24:27], v[164:167], v[172:175], 0
	v_mfma_f32_16x16x32_bf16 v[20:23], v[156:159], v[180:183], 0
	v_mfma_f32_16x16x32_bf16 v[16:19], v[164:167], v[180:183], 0
	v_mfma_f32_16x16x32_bf16 v[12:15], v[156:159], v[188:191], 0
	v_mfma_f32_16x16x32_bf16 v[8:11], v[164:167], v[188:191], 0
	v_mfma_f32_16x16x32_bf16 v[4:7], v[156:159], v[198:201], 0
	v_mfma_f32_16x16x32_bf16 v[0:3], v[164:167], v[198:201], 0
	v_mfma_f32_16x16x32_bf16 v[28:31], v[160:163], v[176:179], v[28:31]
	v_mfma_f32_16x16x32_bf16 v[24:27], v[168:171], v[176:179], v[24:27]
	v_mfma_f32_16x16x32_bf16 v[20:23], v[160:163], v[184:187], v[20:23]
	v_mfma_f32_16x16x32_bf16 v[16:19], v[168:171], v[184:187], v[16:19]
	v_mfma_f32_16x16x32_bf16 v[12:15], v[160:163], v[194:197], v[12:15]
	v_mfma_f32_16x16x32_bf16 v[8:11], v[168:171], v[194:197], v[8:11]
	v_mfma_f32_16x16x32_bf16 v[4:7], v[160:163], v[202:205], v[4:7]
	v_mfma_f32_16x16x32_bf16 v[0:3], v[168:171], v[202:205], v[0:3]
	s_setprio 0
	s_barrier
	v_add_u32_e32 v134, 0x18000, v142
	v_add_u32_e32 v135, 0x1c000, v142
	ds_read_b128 v[136:139], v134
	ds_read_b128 v[144:147], v134 offset:1024
	ds_read_b128 v[148:151], v134 offset:2048
	ds_read_b128 v[152:155], v134 offset:3072
	ds_read_b128 v[156:159], v135
	ds_read_b128 v[160:163], v135 offset:1024
	ds_read_b128 v[164:167], v135 offset:2048
	ds_read_b128 v[168:171], v135 offset:3072
	ds_read_b128 v[172:175], v143 offset:32768
	ds_read_b128 v[176:179], v143 offset:33792
	ds_read_b128 v[180:183], v143 offset:34816
	ds_read_b128 v[184:187], v143 offset:35840
	ds_read_b128 v[188:191], v143 offset:36864
	ds_read_b128 v[194:197], v143 offset:37888
	ds_read_b128 v[198:201], v143 offset:38912
	ds_read_b128 v[202:205], v143 offset:39936
	s_add_u32 s34, s61, 0x40100
	s_addc_u32 s35, s66, 0
	s_mov_b32 m0, s46
	s_nop 0
	global_load_lds_dwordx4 v65, s[34:35]
	s_nop 0
	s_mov_b32 m0, s47
	s_nop 0
	global_load_lds_dwordx4 v140, s[34:35]
	s_waitcnt vmcnt(8)
	s_waitcnt lgkmcnt(0)
	s_barrier
	s_setprio 1
	s_waitcnt lgkmcnt(0)
	v_mfma_f32_16x16x32_bf16 v[128:131], v[136:139], v[172:175], v[128:131]
	v_mfma_f32_16x16x32_bf16 v[124:127], v[148:151], v[172:175], v[124:127]
	s_waitcnt lgkmcnt(5)
	v_mfma_f32_16x16x32_bf16 v[120:123], v[136:139], v[180:183], v[120:123]
	v_mfma_f32_16x16x32_bf16 v[116:119], v[148:151], v[180:183], v[116:119]
	s_waitcnt lgkmcnt(3)
	v_mfma_f32_16x16x32_bf16 v[110:113], v[136:139], v[188:191], v[110:113]
	v_mfma_f32_16x16x32_bf16 v[106:109], v[148:151], v[188:191], v[106:109]
	s_waitcnt lgkmcnt(1)
	v_mfma_f32_16x16x32_bf16 v[102:105], v[136:139], v[198:201], v[102:105]
	v_mfma_f32_16x16x32_bf16 v[98:101], v[148:151], v[198:201], v[98:101]
	v_mfma_f32_16x16x32_bf16 v[128:131], v[144:147], v[176:179], v[128:131]
	v_mfma_f32_16x16x32_bf16 v[124:127], v[152:155], v[176:179], v[124:127]
	v_mfma_f32_16x16x32_bf16 v[120:123], v[144:147], v[184:187], v[120:123]
	v_mfma_f32_16x16x32_bf16 v[116:119], v[152:155], v[184:187], v[116:119]
	v_mfma_f32_16x16x32_bf16 v[110:113], v[144:147], v[194:197], v[110:113]
	v_mfma_f32_16x16x32_bf16 v[106:109], v[152:155], v[194:197], v[106:109]
	s_waitcnt lgkmcnt(0)
	v_mfma_f32_16x16x32_bf16 v[102:105], v[144:147], v[202:205], v[102:105]
	v_mfma_f32_16x16x32_bf16 v[98:101], v[152:155], v[202:205], v[98:101]
	s_setprio 0
	s_setprio 1
	v_mfma_f32_16x16x32_bf16 v[94:97], v[156:159], v[172:175], v[94:97]
	v_mfma_f32_16x16x32_bf16 v[90:93], v[164:167], v[172:175], v[90:93]
	v_mfma_f32_16x16x32_bf16 v[86:89], v[156:159], v[180:183], v[86:89]
	v_mfma_f32_16x16x32_bf16 v[82:85], v[164:167], v[180:183], v[82:85]
	v_mfma_f32_16x16x32_bf16 v[78:81], v[156:159], v[188:191], v[78:81]
	v_mfma_f32_16x16x32_bf16 v[74:77], v[164:167], v[188:191], v[74:77]
	v_mfma_f32_16x16x32_bf16 v[70:73], v[156:159], v[198:201], v[70:73]
	v_mfma_f32_16x16x32_bf16 v[66:69], v[164:167], v[198:201], v[66:69]
	v_mfma_f32_16x16x32_bf16 v[94:97], v[160:163], v[176:179], v[94:97]
	v_mfma_f32_16x16x32_bf16 v[90:93], v[168:171], v[176:179], v[90:93]
	v_mfma_f32_16x16x32_bf16 v[86:89], v[160:163], v[184:187], v[86:89]
	v_mfma_f32_16x16x32_bf16 v[82:85], v[168:171], v[184:187], v[82:85]
	v_mfma_f32_16x16x32_bf16 v[78:81], v[160:163], v[194:197], v[78:81]
	v_mfma_f32_16x16x32_bf16 v[74:77], v[168:171], v[194:197], v[74:77]
	v_mfma_f32_16x16x32_bf16 v[70:73], v[160:163], v[202:205], v[70:73]
	v_mfma_f32_16x16x32_bf16 v[66:69], v[168:171], v[202:205], v[66:69]
	s_setprio 0
	s_barrier
	ds_read_b128 v[172:175], v143 offset:49152
	ds_read_b128 v[176:179], v143 offset:50176
	ds_read_b128 v[180:183], v143 offset:51200
	ds_read_b128 v[184:187], v143 offset:52224
	ds_read_b128 v[188:191], v143 offset:53248
	ds_read_b128 v[194:197], v143 offset:54272
	ds_read_b128 v[198:201], v143 offset:55296
	ds_read_b128 v[202:205], v143 offset:56320
	s_add_u32 s34, s15, 0x180
	s_addc_u32 s35, s33, 0
	s_mov_b32 m0, s51
	s_nop 0
	global_load_lds_dwordx4 v114, s[34:35]
	s_nop 0
	s_mov_b32 m0, s52
	s_nop 0
	global_load_lds_dwordx4 v141, s[34:35]
	s_add_u32 s34, s15, 0x40180
	s_addc_u32 s35, s33, 0
	s_mov_b32 m0, s55
	s_nop 0
	global_load_lds_dwordx4 v114, s[34:35]
	s_nop 0
	s_mov_b32 m0, s56
	s_nop 0
	global_load_lds_dwordx4 v141, s[34:35]
	s_nop 0
	s_mov_b32 m0, s53
	s_nop 0
	global_load_lds_dwordx4 v65, s[26:27]
	s_nop 0
	s_mov_b32 m0, s54
	s_nop 0
	global_load_lds_dwordx4 v140, s[26:27]
	s_waitcnt vmcnt(8)
	s_waitcnt lgkmcnt(0)
	s_barrier
	s_setprio 1
	s_waitcnt lgkmcnt(0)
	v_mfma_f32_16x16x32_bf16 v[60:63], v[136:139], v[172:175], v[60:63]
	v_mfma_f32_16x16x32_bf16 v[56:59], v[148:151], v[172:175], v[56:59]
	s_waitcnt lgkmcnt(5)
	v_mfma_f32_16x16x32_bf16 v[52:55], v[136:139], v[180:183], v[52:55]
	v_mfma_f32_16x16x32_bf16 v[48:51], v[148:151], v[180:183], v[48:51]
	s_waitcnt lgkmcnt(3)
	v_mfma_f32_16x16x32_bf16 v[44:47], v[136:139], v[188:191], v[44:47]
	v_mfma_f32_16x16x32_bf16 v[40:43], v[148:151], v[188:191], v[40:43]
	s_waitcnt lgkmcnt(1)
	v_mfma_f32_16x16x32_bf16 v[36:39], v[136:139], v[198:201], v[36:39]
	v_mfma_f32_16x16x32_bf16 v[32:35], v[148:151], v[198:201], v[32:35]
	v_mfma_f32_16x16x32_bf16 v[60:63], v[144:147], v[176:179], v[60:63]
	v_mfma_f32_16x16x32_bf16 v[56:59], v[152:155], v[176:179], v[56:59]
	v_mfma_f32_16x16x32_bf16 v[52:55], v[144:147], v[184:187], v[52:55]
	v_mfma_f32_16x16x32_bf16 v[48:51], v[152:155], v[184:187], v[48:51]
	v_mfma_f32_16x16x32_bf16 v[44:47], v[144:147], v[194:197], v[44:47]
	v_mfma_f32_16x16x32_bf16 v[40:43], v[152:155], v[194:197], v[40:43]
	s_waitcnt lgkmcnt(0)
	v_mfma_f32_16x16x32_bf16 v[36:39], v[144:147], v[202:205], v[36:39]
	v_mfma_f32_16x16x32_bf16 v[32:35], v[152:155], v[202:205], v[32:35]
	s_setprio 0
	s_setprio 1
	v_mfma_f32_16x16x32_bf16 v[28:31], v[156:159], v[172:175], v[28:31]
	v_mfma_f32_16x16x32_bf16 v[24:27], v[164:167], v[172:175], v[24:27]
	v_mfma_f32_16x16x32_bf16 v[20:23], v[156:159], v[180:183], v[20:23]
	v_mfma_f32_16x16x32_bf16 v[16:19], v[164:167], v[180:183], v[16:19]
	v_mfma_f32_16x16x32_bf16 v[12:15], v[156:159], v[188:191], v[12:15]
	v_mfma_f32_16x16x32_bf16 v[8:11], v[164:167], v[188:191], v[8:11]
	v_mfma_f32_16x16x32_bf16 v[4:7], v[156:159], v[198:201], v[4:7]
	v_mfma_f32_16x16x32_bf16 v[0:3], v[164:167], v[198:201], v[0:3]
	v_mfma_f32_16x16x32_bf16 v[28:31], v[160:163], v[176:179], v[28:31]
	v_mfma_f32_16x16x32_bf16 v[24:27], v[168:171], v[176:179], v[24:27]
	v_mfma_f32_16x16x32_bf16 v[20:23], v[160:163], v[184:187], v[20:23]
	v_mfma_f32_16x16x32_bf16 v[16:19], v[168:171], v[184:187], v[16:19]
	v_mfma_f32_16x16x32_bf16 v[12:15], v[160:163], v[194:197], v[12:15]
	v_mfma_f32_16x16x32_bf16 v[8:11], v[168:171], v[194:197], v[8:11]
	v_mfma_f32_16x16x32_bf16 v[4:7], v[160:163], v[202:205], v[4:7]
	v_mfma_f32_16x16x32_bf16 v[0:3], v[168:171], v[202:205], v[0:3]
	s_setprio 0
	s_barrier
	s_add_i32 s13, s13, 2
	s_add_u32 s18, s18, 0x100
	s_addc_u32 s19, s19, 0
	s_cmp_lt_u32 s13, 12
